# gate GEMM work units are single tiles (1024 per layer) instead of pairs: one gate tile for the two-tile in-projection workgroups, finer tail filler; next gate ticket requested during the last epilogue
# speedup vs baseline: 1.0035x; 1.0035x over previous
; #define LAS __attribute__((address_space(3)))
;     __device__ bool next(int i, Unit& u) const { int pm, pn; if (!T.tile(i, pm, pn)) return false; u.ao = (unsigned)pm * (unsigned)(BM * LDA * 2); u.bo = (unsigned)pn * (unsigned)(BM * LDB * 2); u.nt = K / BK; u.pm = pm; u.pn = pn; u.tag = 0; return true; }
;     __device__ bool next(int i, Unit& u) const { int pm, pn; if (!T.tile(i, pm, pn)) return false; u.ao = (unsigned)pm * (unsigned)(BM * LDA * 2); u.bo = (unsigned)pn * (unsigned)(128 * LDB * 2); u.nt = K / BK; u.pm = pm; u.pn = pn; u.tag = 0; return true; }
; __device__ __forceinline__ KA kargs() { KA p = (KA)__builtin_amdgcn_kernarg_segment_ptr(); asm volatile("" : "+s"(p)); return p; }
; template <int lda, int ldb, class Epi, class Sched>
; __device__ __forceinline__ void gemm_phase(LAS unsigned char* lds, int wid, int lane, const char* baseA, const char* baseB, const Sched& S, const Epi& E) {
;     const int tid = wid * 64 + lane, wr = wid >> 2, wc = wid & 3, fr = lane & 15, fq = lane >> 4;
;     unsigned voffA[2], voffB[2]; int gR[2], gC[2];
; #pragma unroll
;     for (int i = 0; i < 2; ++i) { int R, C; stage_rc(tid * 16 + i * 8192, R, C); const int Rb = Epi::PERM ? ((R & ~31) + perm32(R & 31)) : R;
;         voffA[i] = (unsigned)(R * lda + C) * 2u; voffB[i] = (unsigned)(Rb * ldb + C) * 2u; gR[i] = R; gC[i] = C; }
;     __device__ bool next(int i, g8::Unit& u) const { if (i >= cnt) return false; const int id = base + i, pm = id >> 4, pn = id & 15;
;         u.ao = (unsigned)pm * (unsigned)(g8::BM * 512 * 2); u.bo = (unsigned)pn * (unsigned)(g8::BM * 512 * 2); u.nt = 512 / g8::BK; u.pm = pm; u.pn = pn; u.tag = 0; return true; }
; __device__ __forceinline__ void gate_batches(LAS unsigned char* lds, int wv, int l, int max_batches) {
;     const Frame F = make_frame(lds, wv); const KA a = kargs();
;     unsigned* qg = F.ctl + CW_CVQ + l * 16 + 8;
;     volatile LAS int* gslot = (volatile LAS int*)(lds + MISC_OFF + 512);
; #pragma unroll 1
;     for (int nb = 0; nb < max_batches; ++nb) {
;         int bt;
;         if (F.tid == 0) *gslot = (int)__hip_atomic_fetch_add(qg, 1u, __ATOMIC_RELAXED, __HIP_MEMORY_SCOPE_AGENT);
;         __syncthreads(); bt = *gslot; __syncthreads();
;         if (bt >= 512) break;
.LBB0_442:
	s_or_b64 exec, exec, s[38:39]
	s_waitcnt vmcnt(0) lgkmcnt(0)
	s_barrier
	ds_read_b32 v1, v183
	s_movk_i32 s1, 0x3ff
	s_waitcnt lgkmcnt(0)
	s_barrier
	v_cmp_lt_i32_e32 vcc, s1, v1
	v_readfirstlane_b32 s3, v1
	s_cbranch_vccnz .LBB0_460
	v_lshl_add_u32 v5, v0, 4, s27
	v_add_u32_e32 v2, 0x2000, v5
	v_ashrrev_i32_e32 v1, 31, v2
	v_lshrrev_b32_e32 v1, 22, v1
	v_add_u32_e32 v1, v2, v1
	v_ashrrev_i32_e32 v1, 10, v1
	v_mul_i32_i24_e32 v3, 0x400, v1
	v_sub_u32_e32 v2, v2, v3
	v_lshrrev_b32_e32 v3, 4, v2
	v_bitop3_b32 v3, v3, v2, 32 bitop3:0x6c
	v_ashrrev_i32_e32 v2, 31, v3
	v_lshrrev_b32_e32 v2, 26, v2
	s_add_u32 s1, s16, 0xad00000
	v_add_u32_e32 v4, v3, v2
	s_addc_u32 s2, s17, 0
	v_ashrrev_i32_e32 v2, 6, v4
	v_lshlrev_b32_e32 v6, 3, v1
	v_and_b32_e32 v4, 0xffc0, v4
	s_and_b64 s[10:11], s[10:11], exec
	s_mov_b32 s4, 0xbd00000
	v_and_b32_e32 v6, -16, v6
	v_sub_u32_e32 v3, v3, v4
	s_cselect_b32 s4, s4, 0x22900000
	v_add_u32_e32 v6, v2, v6
	v_lshrrev_b16_e32 v4, 7, v3
	s_add_u32 s13, s16, s4
	v_and_b32_e32 v7, 3, v2
	s_mov_b32 s4, 0x3fffe0
	v_lshrrev_b32_e32 v8, 2, v6
	v_lshlrev_b32_e32 v9, 1, v6
	v_and_b32_e32 v4, 1, v4
	v_and_or_b32 v7, v6, s4, v7
	v_and_b32_e32 v8, 4, v8
	v_and_b32_e32 v9, 24, v9
	v_add_u16_e32 v3, v3, v4
	v_mov_b32_e32 v12, 1
	v_or3_b32 v7, v7, v8, v9
	v_lshlrev_b32_e32 v8, 5, v1
	v_ashrrev_i16_sdwa v3, v12, sext(v3) dst_sel:DWORD dst_unused:UNUSED_PAD src0_sel:DWORD src1_sel:BYTE_0
	v_and_b32_e32 v8, 32, v8
	v_bfe_i32 v3, v3, 0, 16
	v_add_lshl_u32 v4, v8, v3, 1
	v_lshl_add_u32 v156, v7, 10, v4
	v_lshl_add_u32 v158, v6, 10, v4
	v_ashrrev_i32_e32 v4, 31, v5
	v_lshrrev_b32_e32 v4, 22, v4
	v_add_u32_e32 v4, v5, v4
	v_ashrrev_i32_e32 v4, 10, v4
	v_mul_i32_i24_e32 v6, 0x400, v4
	v_sub_u32_e32 v5, v5, v6
	v_lshrrev_b32_e32 v6, 4, v5
	v_bitop3_b32 v6, v6, v5, 32 bitop3:0x6c
	v_ashrrev_i32_e32 v5, 31, v6
	v_lshrrev_b32_e32 v5, 26, v5
	v_add_u32_e32 v7, v6, v5
	v_lshlrev_b32_e32 v8, 3, v4
	v_ashrrev_i32_e32 v5, 6, v7
	v_and_b32_e32 v8, -16, v8
	v_add_u32_e32 v8, v5, v8
	v_and_b32_e32 v9, 3, v5
	s_addc_u32 s31, s17, 0
	v_and_or_b32 v9, v8, s4, v9
	v_lshrrev_b32_e32 v10, 2, v8
	v_lshlrev_b32_e32 v11, 1, v8
	v_and_b32_e32 v7, 0xc0, v7
	s_lshl_b32 s4, s3, 1
	v_and_b32_e32 v10, 4, v10
	v_and_b32_e32 v11, 24, v11
	v_sub_u32_e32 v6, v6, v7
	s_ashr_i32 s50, s3, 4
	s_and_b32 s3, s3, 15
	v_or3_b32 v9, v9, v10, v11
	v_lshlrev_b32_e32 v10, 5, v4
	v_ashrrev_i16_sdwa v6, v12, sext(v6) dst_sel:DWORD dst_unused:UNUSED_PAD src0_sel:DWORD src1_sel:BYTE_0
	s_lshl_b32 s4, s3, 18
	s_lshl_b32 s40, s50, 18
	v_and_b32_e32 v10, 32, v10
	v_bfe_i32 v6, v6, 0, 16
	s_add_u32 s44, s13, s4
	v_add_lshl_u32 v7, v10, v6, 1
	s_addc_u32 s45, s31, 0
	s_add_i32 s51, s27, 0x10000
	s_add_i32 s52, s27, 0x12000
	v_lshl_add_u32 v160, v9, 10, v7
	v_mov_b32_e32 v18, v31
	v_mov_b32_e32 v30, 0x7f7f7f7f
	s_mov_b32 m0, s51
	s_add_u32 s14, s44, 0x20000
	s_load_dwordx2 s[10:11], s[34:35], 0x70
	global_load_lds_dwordx4 v160, s[44:45]
	s_mov_b32 m0, s52
	s_addc_u32 s15, s45, 0
	s_add_i32 s53, s27, 0x14000
	s_add_i32 s54, s27, 0x16000
	global_load_lds_dwordx4 v156, s[44:45]
	s_mov_b32 m0, s53
	s_add_u32 s46, s1, s40
	global_load_lds_dwordx4 v160, s[14:15]
	s_mov_b32 m0, s54
	s_addc_u32 s47, s2, 0
	s_add_i32 s55, s27, 0x2000
	v_lshl_add_u32 v162, v8, 10, v7
	global_load_lds_dwordx4 v156, s[14:15]
	s_mov_b32 m0, s27
	s_add_u32 s14, s46, 0x20000
	global_load_lds_dwordx4 v162, s[46:47]
	s_mov_b32 m0, s55
	s_addc_u32 s15, s47, 0
	s_add_i32 s56, s27, 0x4000
	global_load_lds_dwordx4 v158, s[46:47]
	s_mov_b32 m0, s56
	s_add_i32 s57, s27, 0x6000
	global_load_lds_dwordx4 v162, s[14:15]
	s_mov_b32 m0, s57
	v_mov_b32_e32 v251, 1
	global_load_lds_dwordx4 v158, s[14:15]
	v_readlane_b32 s14, v254, 2
	v_readlane_b32 s15, v254, 3
	s_andn2_b64 vcc, exec, s[14:15]
	s_mov_b32 s41, s5
	v_cndmask_b32_e64 v7, 0, 1, s[14:15]
	v_cmp_ne_u32_e64 s[38:39], 1, v7
	s_cbranch_vccnz .LBB0_445
	s_barrier
;     __device__ bool next(int i, Unit& u) const { int pm, pn; if (!T.tile(i, pm, pn)) return false; u.ao = (unsigned)pm * (unsigned)(BM * LDA * 2); u.bo = (unsigned)pn * (unsigned)(BM * LDB * 2); u.nt = K / BK; u.pm = pm; u.pn = pn; u.tag = 0; return true; }
; #define G8_WAIT_V(n) asm volatile("s_waitcnt vmcnt(" #n ")" ::: "memory")
; #define G8_BAR __builtin_amdgcn_s_barrier()
; template <int lda, int ldb, class Epi, class Sched>
; __device__ __forceinline__ void gemm_phase(LAS unsigned char* lds, int wid, int lane, const char* baseA, const char* baseB, const Sched& S, const Epi& E) {
;     const int tid = wid * 64 + lane, wr = wid >> 2, wc = wid & 3, fr = lane & 15, fq = lane >> 4;
;     unsigned voffA[2], voffB[2]; int gR[2], gC[2];
; #pragma unroll
;     for (int i = 0; i < 2; ++i) { int R, C; stage_rc(tid * 16 + i * 8192, R, C); const int Rb = Epi::PERM ? ((R & ~31) + perm32(R & 31)) : R;
;         voffA[i] = (unsigned)(R * lda + C) * 2u; voffB[i] = (unsigned)(Rb * ldb + C) * 2u; gR[i] = R; gC[i] = C; }
;     unsigned goff[2][2], gnxt[2][2];
;     ...
;     const size_t kstep = (size_t)(BK * 2);
;     const size_t hstepA = (size_t)HALF * lda * 2, hstepB = (size_t)HALF * ldb * 2;
;     const unsigned ldsw = (unsigned)wid * 1024u;
;     const int aoff = lds_byte(wr * 64 + fr, fq * 8), boff = lds_byte(wc * 32 + fr, fq * 8);
;     ...
;     G8_STAGE(G8_SB(0, 0), cB, voffB); if constexpr (!Epi::HALFN) { G8_STAGE(G8_SB(0, 1), cB + hstepB, voffB); } G8_STAGE_A(G8_SA(0, 0), cA, 0, false); G8_STAGE_A(G8_SA(0, 1), cA, 1, false);
;     if (wr == 1) G8_BAR;
;     G8_WAIT_V(2); G8_BAR;
;     G8_STAGE(G8_SB(1, 0), cB + kstep, voffB); G8_STAGE_A(G8_SA(1, 0), cA + kstep, 0, false); if constexpr (!Epi::HALFN) { G8_STAGE(G8_SB(1, 1), cB + hstepB + kstep, voffB); }
;     if constexpr (Epi::HALFN) { G8_WAIT_V(4); } else { G8_WAIT_V(6); } G8_BAR;
;     for (;;) {
;         const bool has_next = S.next(ui + 1, nxt);
;         const char* nA = Sched::GATHER ? baseA : (has_next ? baseA + nxt.ao : cA); const char* nB = has_next ? baseB + nxt.bo : cB;
;         if constexpr (Sched::GATHER) { if (has_next) { G8_GOFF(gnxt, nxt); } else { _Pragma("unroll") for (int h_ = 0; h_ < 2; ++h_) _Pragma("unroll") for (int i_ = 0; i_ < 2; ++i_) gnxt[h_][i_] = goff[h_][i_]; } }
;         int nt = cur.nt; asm volatile("" : "+s"(nt));
.LBB0_445:
	s_lshl_b32 s14, s72, 12
	s_ashr_i32 s15, s14, 31
	s_lshl_b64 s[14:15], s[14:15], 2
	s_waitcnt lgkmcnt(0)
	s_add_u32 s42, s10, s14
	s_addc_u32 s43, s11, s15
	v_mbcnt_lo_u32_b32 v149, -1, 0
	v_mbcnt_hi_u32_b32 v149, -1, v149
	s_lshl_b32 s14, s3, 8
	s_or_b32 s14, s14, s95
	v_and_b32_e32 v150, 31, v149
	v_lshrrev_b32_e32 v149, 5, v149
	v_lshl_or_b32 v149, v149, 7, v150
	v_add_lshl_u32 v154, v149, s14, 2
	v_mov_b32_e32 v155, 0
	s_lshr_b32 s14, s27, 1
	s_add_i32 s14, s14, 0x23000
	v_lshl_add_u64 v[154:155], s[42:43], 0, v[154:155]
	s_mov_b32 m0, s14
	s_nop 0
	global_load_lds_dword v[154:155], off
	v_mov_b32_e32 v161, v31
	s_add_u32 s10, s16, 0x16900000
	v_mov_b32_e32 v157, v31
	v_lshl_add_u64 v[8:9], s[44:45], 0, v[160:161]
	s_addc_u32 s11, s17, 0
	s_add_i32 s58, s27, 0x18000
	v_mov_b32_e32 v163, v31
	v_lshl_add_u64 v[10:11], s[44:45], 0, v[156:157]
	v_lshl_add_u64 v[8:9], v[8:9], 0, s[22:23]
	s_mov_b32 m0, s58
	s_add_i32 s59, s27, 0x1a000
	v_mov_b32_e32 v159, v31
	v_lshl_add_u64 v[12:13], s[46:47], 0, v[162:163]
	s_waitcnt vmcnt(3)
	s_barrier
	global_load_lds_dwordx4 v[8:9], off
	v_lshl_add_u64 v[8:9], v[10:11], 0, s[22:23]
	s_mov_b32 m0, s59
	s_add_i32 s60, s27, 0x8000
	s_add_i32 s61, s27, 0xa000
	v_lshl_add_u64 v[14:15], s[46:47], 0, v[158:159]
	global_load_lds_dwordx4 v[8:9], off
	v_lshl_add_u64 v[8:9], v[12:13], 0, s[22:23]
	s_mov_b32 m0, s60
	s_add_u32 s14, s44, 0x20080
	global_load_lds_dwordx4 v[8:9], off
	v_lshl_add_u64 v[8:9], v[14:15], 0, s[22:23]
	s_mov_b32 m0, s61
	s_addc_u32 s15, s45, 0
	s_add_i32 s62, s27, 0x1c000
	global_load_lds_dwordx4 v[8:9], off
	v_lshl_add_u64 v[8:9], s[14:15], 0, v[160:161]
	s_mov_b32 m0, s62
	s_add_i32 s63, s27, 0x1e000
	global_load_lds_dwordx4 v[8:9], off
	v_lshl_add_u64 v[8:9], s[14:15], 0, v[156:157]
	s_mov_b32 m0, s63
	v_and_b32_e32 v7, 15, v0
	global_load_lds_dwordx4 v[8:9], off
	v_or_b32_e32 v8, s9, v7
	v_lshlrev_b32_e32 v10, 6, v8
	v_and_b32_e32 v11, 48, v0
	s_movk_i32 s4, 0x3c0
	v_lshrrev_b32_e32 v9, 6, v0
	v_and_or_b32 v10, v10, s4, v11
	v_readlane_b32 s4, v254, 8
	v_lshlrev_b32_e32 v0, 2, v0
	v_lshlrev_b32_e32 v12, 10, v9
	v_lshl_or_b32 v7, v7, 6, v11
	v_add_lshl_u32 v9, v9, s4, 10
	v_and_b32_e32 v0, 32, v0
	v_bitop3_b32 v0, v7, v9, v0 bitop3:0xde
	v_or_b32_e32 v148, 0x10000, v0
	v_add_u32_e32 v151, 0x14000, v0
	v_or_b32_e32 v176, 0x18000, v0
	v_add_u32_e32 v177, 0x1c000, v0
	v_add_u32_e32 v178, 0x10400, v0
	v_add_u32_e32 v179, 0x10800, v0
	v_add_u32_e32 v180, 0x10c00, v0
	v_add_u32_e32 v181, 0x14400, v0
	v_add_u32_e32 v205, 0x14800, v0
	v_add_u32_e32 v206, 0x14c00, v0
	v_add_u32_e32 v207, 0x18400, v0
	v_add_u32_e32 v208, 0x18800, v0
	v_add_u32_e32 v209, 0x18c00, v0
	v_add_u32_e32 v210, 0x1c400, v0
	v_add_u32_e32 v211, 0x1c800, v0
	v_add_u32_e32 v212, 0x1cc00, v0
	v_lshlrev_b32_e32 v0, 13, v1
	v_and_b32_e32 v0, 0xffffc000, v0
	v_lshl_add_u32 v0, v2, 10, v0
	v_and_b32_e32 v1, 1, v1
	v_lshl_or_b32 v0, v1, 6, v0
	v_lshl_add_u32 v164, v3, 1, v0
	v_lshlrev_b32_e32 v0, 13, v4
	v_lshlrev_b32_e32 v8, 2, v8
	v_and_b32_e32 v0, 0xffffc000, v0
	v_and_b32_e32 v8, 32, v8
	s_waitcnt vmcnt(7)
	v_lshl_add_u32 v0, v5, 10, v0
	v_and_b32_e32 v1, 1, v4
	v_bitop3_b32 v7, v10, v12, v8 bitop3:0xde
	s_or_b32 s64, s3, 1
	v_lshl_or_b32 v0, v1, 6, v0
	v_readlane_b32 s4, v253, 61
	v_mov_b32_e32 v19, v18
	v_mov_b32_e32 v20, v18
	v_mov_b32_e32 v21, v18
	s_lshl_b32 s65, s64, 18
	v_mov_b32_e32 v165, v31
	v_lshl_add_u32 v166, v6, 1, v0
	v_mov_b32_e32 v167, v31
	s_mov_b64 s[14:15], 0
	v_add_u32_e32 v213, s4, v7
	s_mov_b32 s21, s3
	s_mov_b32 s28, s50
	s_lshl_b32 s29, s3, 18
	s_mov_b32 s4, s40
	s_mov_b32 s20, s50
	v_mov_b32_e32 v16, v18
	s_barrier
	s_branch .LBB0_448

; __device__ __forceinline__ float fast_sigmoid(float z) { return __builtin_amdgcn_rcpf(1.f + __builtin_amdgcn_exp2f(-z * LOG2E)); }
;     static __device__ __forceinline__ unsigned q8(float z) { return (unsigned)(fast_sigmoid(z) * 255.f + 0.5f); }
;     __device__ __forceinline__ void operator()(const f32x4 (&acc)[2][2][4][2], const g8::Unit& u, int wr, int wc, int fr, int fq) const {
;         const int row0 = u.pm * 256 + wr * 64 + fr, col0 = u.pn * 256 + wc * 32 + 8 * fq;
; #pragma unroll
;         for (int bj = 0; bj < 2; ++bj) {
;             const f32x4 bv0 = *(const f32x4*)(bgate + col0 + bj * 128), bv1 = *(const f32x4*)(bgate + col0 + bj * 128 + 4);
; #pragma unroll
;             for (int ai = 0; ai < 2; ++ai)
; #pragma unroll
;                 for (int m = 0; m < 4; ++m) { const int row = row0 + ai * 128 + m * 16; unsigned char* rp = GT + (size_t)row * 4096 + col0 + bj * 128;
;                     const f32x4 v0 = acc[ai][bj][m][0] * 0.03125f + bv0, v1 = acc[ai][bj][m][1] * 0.03125f + bv1;
;                     u32x2 w; w.x = q8(v0[0]) | (q8(v0[1]) << 8) | (q8(v0[2]) << 16) | (q8(v0[3]) << 24); w.y = q8(v1[0]) | (q8(v1[1]) << 8) | (q8(v1[2]) << 16) | (q8(v1[3]) << 24);
;                     *(u32x2*)rp = w; } }
.LBB0_455:
	s_mov_b32 s4, -1
	s_mov_b32 s44, 0
	s_lshr_b32 s45, s27, 1
	s_lshl_b32 s44, s44, 8
	s_add_i32 s45, s45, 0x23000
	s_add_i32 s44, s44, s45
	s_lshl_b32 s3, s3, 8
	v_mbcnt_lo_u32_b32 v0, s4, 0
	v_mbcnt_hi_u32_b32 v0, s4, v0
	s_lshl_b32 s4, s20, 8
	s_add_i32 s4, s4, s9
	v_lshrrev_b32_e32 v168, 2, v0
	v_and_b32_e32 v170, 3, v0
	v_and_b32_e32 v17, 60, v0
	v_or_b32_e32 v168, s4, v168
	v_lshrrev_b32_e32 v0, 1, v0
	s_or_b32 s3, s3, s95
	v_lshl_or_b32 v17, v170, 6, v17
	v_and_b32_e32 v0, 56, v0
	v_lshl_add_u32 v170, v170, 3, s3
	v_lshl_add_u32 v12, v0, 2, s44
	ds_read_b128 v[4:7], v12
	ds_read_b128 v[0:3], v12 offset:16
	ds_read_b128 v[214:217], v12 offset:128
	ds_read_b128 v[218:221], v12 offset:144
	v_ashrrev_i32_e32 v171, 31, v170
	v_ashrrev_i32_e32 v169, 31, v168
	v_lshlrev_b64 v[8:9], 12, v[168:169]
	s_mov_b64 s[44:45], 0x10000
	s_mov_b64 vcc, 0x80000
	v_lshl_add_u64 v[8:9], s[10:11], 0, v[8:9]
	s_mov_b32 s20, 0xbd38aa3b
	s_mov_b32 s21, 0x3b808081
	v_lshl_add_u64 v[8:9], v[8:9], 0, v[170:171]
	v_lshl_add_u64 v[10:11], v[8:9], 0, s[44:45]
	v_lshl_add_u64 v[222:223], v[8:9], 0, vcc
	v_lshl_add_u64 v[14:15], v[10:11], 0, s[44:45]
	v_lshl_add_u64 v[224:225], v[222:223], 0, s[44:45]
	v_lshl_add_u64 v[168:169], v[14:15], 0, s[44:45]
	v_lshl_add_u64 v[226:227], v[224:225], 0, s[44:45]
	v_lshl_add_u64 v[228:229], v[226:227], 0, s[44:45]
	s_waitcnt lgkmcnt(0)
	v_mul_f32_e32 v0, 0xbfb8aa3b, v0
	v_mul_f32_e32 v1, 0xbfb8aa3b, v1
	v_mul_f32_e32 v2, 0xbfb8aa3b, v2
	v_mul_f32_e32 v3, 0xbfb8aa3b, v3
	v_mul_f32_e32 v4, 0xbfb8aa3b, v4
	v_mul_f32_e32 v5, 0xbfb8aa3b, v5
	v_mul_f32_e32 v6, 0xbfb8aa3b, v6
	v_mul_f32_e32 v7, 0xbfb8aa3b, v7
	v_mul_f32_e32 v214, 0xbfb8aa3b, v214
	v_mul_f32_e32 v215, 0xbfb8aa3b, v215
	v_mul_f32_e32 v216, 0xbfb8aa3b, v216
	v_mul_f32_e32 v217, 0xbfb8aa3b, v217
	v_mul_f32_e32 v218, 0xbfb8aa3b, v218
	v_mul_f32_e32 v219, 0xbfb8aa3b, v219
	v_mul_f32_e32 v220, 0xbfb8aa3b, v220
	v_mul_f32_e32 v221, 0xbfb8aa3b, v221
	v_pk_fma_f32 v[144:145], v[144:145], s[20:21], v[4:5] op_sel_hi:[1,0,1]
	v_pk_fma_f32 v[146:147], v[146:147], s[20:21], v[6:7] op_sel_hi:[1,0,1]
	v_pk_fma_f32 v[140:141], v[140:141], s[20:21], v[0:1] op_sel_hi:[1,0,1]
	v_pk_fma_f32 v[142:143], v[142:143], s[20:21], v[2:3] op_sel_hi:[1,0,1]
	v_pk_fma_f32 v[136:137], v[136:137], s[20:21], v[4:5] op_sel_hi:[1,0,1]
	v_pk_fma_f32 v[138:139], v[138:139], s[20:21], v[6:7] op_sel_hi:[1,0,1]
	v_pk_fma_f32 v[132:133], v[132:133], s[20:21], v[0:1] op_sel_hi:[1,0,1]
	v_pk_fma_f32 v[134:135], v[134:135], s[20:21], v[2:3] op_sel_hi:[1,0,1]
	v_exp_f32_e32 v144, v144
	v_exp_f32_e32 v145, v145
	v_exp_f32_e32 v146, v146
	v_exp_f32_e32 v147, v147
	v_exp_f32_e32 v140, v140
	v_exp_f32_e32 v141, v141
	v_exp_f32_e32 v142, v142
	v_exp_f32_e32 v143, v143
	v_exp_f32_e32 v136, v136
	v_exp_f32_e32 v137, v137
	v_exp_f32_e32 v138, v138
	v_exp_f32_e32 v139, v139
	v_exp_f32_e32 v132, v132
	v_exp_f32_e32 v133, v133
	v_exp_f32_e32 v134, v134
	v_exp_f32_e32 v135, v135
	v_fma_f32 v144, v144, s21, s21
	v_fma_f32 v145, v145, s21, s21
	v_fma_f32 v146, v146, s21, s21
	v_fma_f32 v147, v147, s21, s21
	v_fma_f32 v140, v140, s21, s21
	v_fma_f32 v141, v141, s21, s21
	v_fma_f32 v142, v142, s21, s21
	v_fma_f32 v143, v143, s21, s21
	v_fma_f32 v136, v136, s21, s21
	v_fma_f32 v137, v137, s21, s21
	v_fma_f32 v138, v138, s21, s21
	v_fma_f32 v139, v139, s21, s21
	v_fma_f32 v132, v132, s21, s21
	v_fma_f32 v133, v133, s21, s21
	v_fma_f32 v134, v134, s21, s21
	v_fma_f32 v135, v135, s21, s21
	v_rcp_f32_e32 v144, v144
	v_rcp_f32_e32 v145, v145
	v_rcp_f32_e32 v146, v146
	v_rcp_f32_e32 v147, v147
	v_rcp_f32_e32 v140, v140
	v_rcp_f32_e32 v141, v141
	v_rcp_f32_e32 v142, v142
	v_rcp_f32_e32 v143, v143
	v_rcp_f32_e32 v136, v136
	v_rcp_f32_e32 v137, v137
	v_rcp_f32_e32 v138, v138
	v_rcp_f32_e32 v139, v139
	v_rcp_f32_e32 v132, v132
	v_rcp_f32_e32 v133, v133
	v_rcp_f32_e32 v134, v134
	v_rcp_f32_e32 v135, v135
	v_cvt_rpi_i32_f32_e32 v144, v144
	v_cvt_rpi_i32_f32_e32 v136, v136
	v_cvt_rpi_i32_f32_sdwa v144, v145 dst_sel:BYTE_1 dst_unused:UNUSED_PRESERVE src0_sel:DWORD
	v_cvt_rpi_i32_f32_sdwa v136, v137 dst_sel:BYTE_1 dst_unused:UNUSED_PRESERVE src0_sel:DWORD
	v_cvt_rpi_i32_f32_e32 v145, v140
	v_cvt_rpi_i32_f32_e32 v137, v132
	v_cvt_rpi_i32_f32_sdwa v144, v146 dst_sel:BYTE_2 dst_unused:UNUSED_PRESERVE src0_sel:DWORD
	v_cvt_rpi_i32_f32_sdwa v136, v138 dst_sel:BYTE_2 dst_unused:UNUSED_PRESERVE src0_sel:DWORD
	v_cvt_rpi_i32_f32_sdwa v145, v141 dst_sel:BYTE_1 dst_unused:UNUSED_PRESERVE src0_sel:DWORD
	v_cvt_rpi_i32_f32_sdwa v137, v133 dst_sel:BYTE_1 dst_unused:UNUSED_PRESERVE src0_sel:DWORD
	v_cvt_rpi_i32_f32_sdwa v144, v147 dst_sel:BYTE_3 dst_unused:UNUSED_PRESERVE src0_sel:DWORD
	v_cvt_rpi_i32_f32_sdwa v136, v139 dst_sel:BYTE_3 dst_unused:UNUSED_PRESERVE src0_sel:DWORD
	v_cvt_rpi_i32_f32_sdwa v145, v142 dst_sel:BYTE_2 dst_unused:UNUSED_PRESERVE src0_sel:DWORD
	v_cvt_rpi_i32_f32_sdwa v137, v134 dst_sel:BYTE_2 dst_unused:UNUSED_PRESERVE src0_sel:DWORD
	v_cvt_rpi_i32_f32_sdwa v145, v143 dst_sel:BYTE_3 dst_unused:UNUSED_PRESERVE src0_sel:DWORD
	v_cvt_rpi_i32_f32_sdwa v137, v135 dst_sel:BYTE_3 dst_unused:UNUSED_PRESERVE src0_sel:DWORD
	ds_bpermute_b32 v144, v17, v144
	ds_bpermute_b32 v145, v17, v145
	ds_bpermute_b32 v136, v17, v136
	ds_bpermute_b32 v137, v17, v137
	v_pk_fma_f32 v[128:129], v[128:129], s[20:21], v[4:5] op_sel_hi:[1,0,1]
	v_pk_fma_f32 v[130:131], v[130:131], s[20:21], v[6:7] op_sel_hi:[1,0,1]
	v_pk_fma_f32 v[124:125], v[124:125], s[20:21], v[0:1] op_sel_hi:[1,0,1]
	v_pk_fma_f32 v[126:127], v[126:127], s[20:21], v[2:3] op_sel_hi:[1,0,1]
	v_pk_fma_f32 v[120:121], v[120:121], s[20:21], v[4:5] op_sel_hi:[1,0,1]
; __device__ __forceinline__ float fast_sigmoid(float z) { return __builtin_amdgcn_rcpf(1.f + __builtin_amdgcn_exp2f(-z * LOG2E)); }
;     static __device__ __forceinline__ unsigned q8(float z) { return (unsigned)(fast_sigmoid(z) * 255.f + 0.5f); }
;     __device__ __forceinline__ void operator()(const f32x4 (&acc)[2][2][4][2], const g8::Unit& u, int wr, int wc, int fr, int fq) const {
;         const int row0 = u.pm * 256 + wr * 64 + fr, col0 = u.pn * 256 + wc * 32 + 8 * fq;
; #pragma unroll
;         for (int bj = 0; bj < 2; ++bj) {
;             const f32x4 bv0 = *(const f32x4*)(bgate + col0 + bj * 128), bv1 = *(const f32x4*)(bgate + col0 + bj * 128 + 4);
; #pragma unroll
;             for (int ai = 0; ai < 2; ++ai)
; #pragma unroll
;                 for (int m = 0; m < 4; ++m) { const int row = row0 + ai * 128 + m * 16; unsigned char* rp = GT + (size_t)row * 4096 + col0 + bj * 128;
;                     const f32x4 v0 = acc[ai][bj][m][0] * 0.03125f + bv0, v1 = acc[ai][bj][m][1] * 0.03125f + bv1;
;                     u32x2 w; w.x = q8(v0[0]) | (q8(v0[1]) << 8) | (q8(v0[2]) << 16) | (q8(v0[3]) << 24); w.y = q8(v1[0]) | (q8(v1[1]) << 8) | (q8(v1[2]) << 16) | (q8(v1[3]) << 24);
;                     *(u32x2*)rp = w; } }
	v_pk_fma_f32 v[122:123], v[122:123], s[20:21], v[6:7] op_sel_hi:[1,0,1]
	v_pk_fma_f32 v[116:117], v[116:117], s[20:21], v[0:1] op_sel_hi:[1,0,1]
	v_pk_fma_f32 v[118:119], v[118:119], s[20:21], v[2:3] op_sel_hi:[1,0,1]
	v_exp_f32_e32 v128, v128
	v_exp_f32_e32 v129, v129
	v_exp_f32_e32 v130, v130
	v_exp_f32_e32 v131, v131
	v_exp_f32_e32 v124, v124
	v_exp_f32_e32 v125, v125
	v_exp_f32_e32 v126, v126
	v_exp_f32_e32 v127, v127
	v_exp_f32_e32 v120, v120
	v_exp_f32_e32 v121, v121
	v_exp_f32_e32 v122, v122
	v_exp_f32_e32 v123, v123
	v_exp_f32_e32 v116, v116
	v_exp_f32_e32 v117, v117
	v_exp_f32_e32 v118, v118
	v_exp_f32_e32 v119, v119
	v_fma_f32 v128, v128, s21, s21
	v_fma_f32 v129, v129, s21, s21
	v_fma_f32 v130, v130, s21, s21
	v_fma_f32 v131, v131, s21, s21
	v_fma_f32 v124, v124, s21, s21
	v_fma_f32 v125, v125, s21, s21
	v_fma_f32 v126, v126, s21, s21
	v_fma_f32 v127, v127, s21, s21
	v_fma_f32 v120, v120, s21, s21
	v_fma_f32 v121, v121, s21, s21
	v_fma_f32 v122, v122, s21, s21
	v_fma_f32 v123, v123, s21, s21
	v_fma_f32 v116, v116, s21, s21
	v_fma_f32 v117, v117, s21, s21
	v_fma_f32 v118, v118, s21, s21
	v_fma_f32 v119, v119, s21, s21
	v_rcp_f32_e32 v128, v128
	v_rcp_f32_e32 v129, v129
	v_rcp_f32_e32 v130, v130
	v_rcp_f32_e32 v131, v131
	v_rcp_f32_e32 v124, v124
	v_rcp_f32_e32 v125, v125
	v_rcp_f32_e32 v126, v126
	v_rcp_f32_e32 v127, v127
	v_rcp_f32_e32 v120, v120
	v_rcp_f32_e32 v121, v121
	v_rcp_f32_e32 v122, v122
	v_rcp_f32_e32 v123, v123
	v_rcp_f32_e32 v116, v116
	v_rcp_f32_e32 v117, v117
	v_rcp_f32_e32 v118, v118
	v_rcp_f32_e32 v119, v119
	v_cvt_rpi_i32_f32_e32 v128, v128
	v_cvt_rpi_i32_f32_e32 v120, v120
	v_cvt_rpi_i32_f32_sdwa v128, v129 dst_sel:BYTE_1 dst_unused:UNUSED_PRESERVE src0_sel:DWORD
	v_cvt_rpi_i32_f32_sdwa v120, v121 dst_sel:BYTE_1 dst_unused:UNUSED_PRESERVE src0_sel:DWORD
	v_cvt_rpi_i32_f32_e32 v129, v124
	v_cvt_rpi_i32_f32_e32 v121, v116
	v_cvt_rpi_i32_f32_sdwa v128, v130 dst_sel:BYTE_2 dst_unused:UNUSED_PRESERVE src0_sel:DWORD
	v_cvt_rpi_i32_f32_sdwa v120, v122 dst_sel:BYTE_2 dst_unused:UNUSED_PRESERVE src0_sel:DWORD
	v_cvt_rpi_i32_f32_sdwa v129, v125 dst_sel:BYTE_1 dst_unused:UNUSED_PRESERVE src0_sel:DWORD
	v_cvt_rpi_i32_f32_sdwa v121, v117 dst_sel:BYTE_1 dst_unused:UNUSED_PRESERVE src0_sel:DWORD
	v_cvt_rpi_i32_f32_sdwa v128, v131 dst_sel:BYTE_3 dst_unused:UNUSED_PRESERVE src0_sel:DWORD
	v_cvt_rpi_i32_f32_sdwa v120, v123 dst_sel:BYTE_3 dst_unused:UNUSED_PRESERVE src0_sel:DWORD
	v_cvt_rpi_i32_f32_sdwa v129, v126 dst_sel:BYTE_2 dst_unused:UNUSED_PRESERVE src0_sel:DWORD
	v_cvt_rpi_i32_f32_sdwa v121, v118 dst_sel:BYTE_2 dst_unused:UNUSED_PRESERVE src0_sel:DWORD
	v_cvt_rpi_i32_f32_sdwa v129, v127 dst_sel:BYTE_3 dst_unused:UNUSED_PRESERVE src0_sel:DWORD
	v_cvt_rpi_i32_f32_sdwa v121, v119 dst_sel:BYTE_3 dst_unused:UNUSED_PRESERVE src0_sel:DWORD
	ds_bpermute_b32 v128, v17, v128
	ds_bpermute_b32 v129, v17, v129
	ds_bpermute_b32 v120, v17, v120
	ds_bpermute_b32 v121, v17, v121
	s_waitcnt lgkmcnt(4)
	global_store_dwordx2 v[8:9], v[144:145], off
	global_store_dwordx2 v[10:11], v[136:137], off
	v_pk_fma_f32 v[112:113], v[112:113], s[20:21], v[4:5] op_sel_hi:[1,0,1]
	v_pk_fma_f32 v[114:115], v[114:115], s[20:21], v[6:7] op_sel_hi:[1,0,1]
	v_pk_fma_f32 v[108:109], v[108:109], s[20:21], v[0:1] op_sel_hi:[1,0,1]
	v_pk_fma_f32 v[110:111], v[110:111], s[20:21], v[2:3] op_sel_hi:[1,0,1]
	v_pk_fma_f32 v[104:105], v[104:105], s[20:21], v[4:5] op_sel_hi:[1,0,1]
	v_pk_fma_f32 v[106:107], v[106:107], s[20:21], v[6:7] op_sel_hi:[1,0,1]
	v_pk_fma_f32 v[100:101], v[100:101], s[20:21], v[0:1] op_sel_hi:[1,0,1]
	v_pk_fma_f32 v[102:103], v[102:103], s[20:21], v[2:3] op_sel_hi:[1,0,1]
	v_exp_f32_e32 v112, v112
	v_exp_f32_e32 v113, v113
	v_exp_f32_e32 v114, v114
	v_exp_f32_e32 v115, v115
	v_exp_f32_e32 v108, v108
	v_exp_f32_e32 v109, v109
	v_exp_f32_e32 v110, v110
	v_exp_f32_e32 v111, v111
	v_exp_f32_e32 v104, v104
	v_exp_f32_e32 v105, v105
	v_exp_f32_e32 v106, v106
	v_exp_f32_e32 v107, v107
	v_exp_f32_e32 v100, v100
	v_exp_f32_e32 v101, v101
	v_exp_f32_e32 v102, v102
	v_exp_f32_e32 v103, v103
	v_fma_f32 v112, v112, s21, s21
	v_fma_f32 v113, v113, s21, s21
	v_fma_f32 v114, v114, s21, s21
	v_fma_f32 v115, v115, s21, s21
	v_fma_f32 v108, v108, s21, s21
	v_fma_f32 v109, v109, s21, s21
	v_fma_f32 v110, v110, s21, s21
	v_fma_f32 v111, v111, s21, s21
	v_fma_f32 v104, v104, s21, s21
	v_fma_f32 v105, v105, s21, s21
	v_fma_f32 v106, v106, s21, s21
	v_fma_f32 v107, v107, s21, s21
	v_fma_f32 v100, v100, s21, s21
	v_fma_f32 v101, v101, s21, s21
	v_fma_f32 v102, v102, s21, s21
	v_fma_f32 v103, v103, s21, s21
	v_rcp_f32_e32 v112, v112
	v_rcp_f32_e32 v113, v113
	v_rcp_f32_e32 v114, v114
	v_rcp_f32_e32 v115, v115
	v_rcp_f32_e32 v108, v108
	v_rcp_f32_e32 v109, v109
	v_rcp_f32_e32 v110, v110
	v_rcp_f32_e32 v111, v111
	v_rcp_f32_e32 v104, v104
	v_rcp_f32_e32 v105, v105
	v_rcp_f32_e32 v106, v106
	v_rcp_f32_e32 v107, v107
	v_rcp_f32_e32 v100, v100
	v_rcp_f32_e32 v101, v101
	v_rcp_f32_e32 v102, v102
	v_rcp_f32_e32 v103, v103
	v_cvt_rpi_i32_f32_e32 v112, v112
	v_cvt_rpi_i32_f32_e32 v104, v104
	v_cvt_rpi_i32_f32_sdwa v112, v113 dst_sel:BYTE_1 dst_unused:UNUSED_PRESERVE src0_sel:DWORD
	v_cvt_rpi_i32_f32_sdwa v104, v105 dst_sel:BYTE_1 dst_unused:UNUSED_PRESERVE src0_sel:DWORD
	v_cvt_rpi_i32_f32_e32 v113, v108
	v_cvt_rpi_i32_f32_e32 v105, v100
	v_cvt_rpi_i32_f32_sdwa v112, v114 dst_sel:BYTE_2 dst_unused:UNUSED_PRESERVE src0_sel:DWORD
	v_cvt_rpi_i32_f32_sdwa v104, v106 dst_sel:BYTE_2 dst_unused:UNUSED_PRESERVE src0_sel:DWORD
	v_cvt_rpi_i32_f32_sdwa v113, v109 dst_sel:BYTE_1 dst_unused:UNUSED_PRESERVE src0_sel:DWORD
	v_cvt_rpi_i32_f32_sdwa v105, v101 dst_sel:BYTE_1 dst_unused:UNUSED_PRESERVE src0_sel:DWORD
	v_cvt_rpi_i32_f32_sdwa v112, v115 dst_sel:BYTE_3 dst_unused:UNUSED_PRESERVE src0_sel:DWORD
	v_cvt_rpi_i32_f32_sdwa v104, v107 dst_sel:BYTE_3 dst_unused:UNUSED_PRESERVE src0_sel:DWORD
	v_cvt_rpi_i32_f32_sdwa v113, v110 dst_sel:BYTE_2 dst_unused:UNUSED_PRESERVE src0_sel:DWORD
	v_cvt_rpi_i32_f32_sdwa v105, v102 dst_sel:BYTE_2 dst_unused:UNUSED_PRESERVE src0_sel:DWORD
	v_cvt_rpi_i32_f32_sdwa v113, v111 dst_sel:BYTE_3 dst_unused:UNUSED_PRESERVE src0_sel:DWORD
	v_cvt_rpi_i32_f32_sdwa v105, v103 dst_sel:BYTE_3 dst_unused:UNUSED_PRESERVE src0_sel:DWORD
	ds_bpermute_b32 v112, v17, v112
	ds_bpermute_b32 v113, v17, v113
	ds_bpermute_b32 v104, v17, v104
	ds_bpermute_b32 v105, v17, v105
	s_waitcnt lgkmcnt(4)
; __device__ __forceinline__ float fast_sigmoid(float z) { return __builtin_amdgcn_rcpf(1.f + __builtin_amdgcn_exp2f(-z * LOG2E)); }
;     static __device__ __forceinline__ unsigned q8(float z) { return (unsigned)(fast_sigmoid(z) * 255.f + 0.5f); }
;     __device__ __forceinline__ void operator()(const f32x4 (&acc)[2][2][4][2], const g8::Unit& u, int wr, int wc, int fr, int fq) const {
;         const int row0 = u.pm * 256 + wr * 64 + fr, col0 = u.pn * 256 + wc * 32 + 8 * fq;
; #pragma unroll
;         for (int bj = 0; bj < 2; ++bj) {
;             const f32x4 bv0 = *(const f32x4*)(bgate + col0 + bj * 128), bv1 = *(const f32x4*)(bgate + col0 + bj * 128 + 4);
; #pragma unroll
;             for (int ai = 0; ai < 2; ++ai)
; #pragma unroll
;                 for (int m = 0; m < 4; ++m) { const int row = row0 + ai * 128 + m * 16; unsigned char* rp = GT + (size_t)row * 4096 + col0 + bj * 128;
;                     const f32x4 v0 = acc[ai][bj][m][0] * 0.03125f + bv0, v1 = acc[ai][bj][m][1] * 0.03125f + bv1;
;                     u32x2 w; w.x = q8(v0[0]) | (q8(v0[1]) << 8) | (q8(v0[2]) << 16) | (q8(v0[3]) << 24); w.y = q8(v1[0]) | (q8(v1[1]) << 8) | (q8(v1[2]) << 16) | (q8(v1[3]) << 24);
;                     *(u32x2*)rp = w; } }
	global_store_dwordx2 v[14:15], v[128:129], off
	global_store_dwordx2 v[168:169], v[120:121], off
	v_pk_fma_f32 v[96:97], v[96:97], s[20:21], v[4:5] op_sel_hi:[1,0,1]
	v_pk_fma_f32 v[98:99], v[98:99], s[20:21], v[6:7] op_sel_hi:[1,0,1]
	v_pk_fma_f32 v[92:93], v[92:93], s[20:21], v[0:1] op_sel_hi:[1,0,1]
	v_pk_fma_f32 v[94:95], v[94:95], s[20:21], v[2:3] op_sel_hi:[1,0,1]
	v_pk_fma_f32 v[88:89], v[88:89], s[20:21], v[4:5] op_sel_hi:[1,0,1]
	v_pk_fma_f32 v[90:91], v[90:91], s[20:21], v[6:7] op_sel_hi:[1,0,1]
	v_pk_fma_f32 v[84:85], v[84:85], s[20:21], v[0:1] op_sel_hi:[1,0,1]
	v_pk_fma_f32 v[86:87], v[86:87], s[20:21], v[2:3] op_sel_hi:[1,0,1]
	v_exp_f32_e32 v96, v96
	v_exp_f32_e32 v97, v97
	v_exp_f32_e32 v98, v98
	v_exp_f32_e32 v99, v99
	v_exp_f32_e32 v92, v92
	v_exp_f32_e32 v93, v93
	v_exp_f32_e32 v94, v94
	v_exp_f32_e32 v95, v95
	v_exp_f32_e32 v88, v88
	v_exp_f32_e32 v89, v89
	v_exp_f32_e32 v90, v90
	v_exp_f32_e32 v91, v91
	v_exp_f32_e32 v84, v84
	v_exp_f32_e32 v85, v85
	v_exp_f32_e32 v86, v86
	v_exp_f32_e32 v87, v87
	v_fma_f32 v96, v96, s21, s21
	v_fma_f32 v97, v97, s21, s21
	v_fma_f32 v98, v98, s21, s21
	v_fma_f32 v99, v99, s21, s21
	v_fma_f32 v92, v92, s21, s21
	v_fma_f32 v93, v93, s21, s21
	v_fma_f32 v94, v94, s21, s21
	v_fma_f32 v95, v95, s21, s21
	v_fma_f32 v88, v88, s21, s21
	v_fma_f32 v89, v89, s21, s21
	v_fma_f32 v90, v90, s21, s21
	v_fma_f32 v91, v91, s21, s21
	v_fma_f32 v84, v84, s21, s21
	v_fma_f32 v85, v85, s21, s21
	v_fma_f32 v86, v86, s21, s21
	v_fma_f32 v87, v87, s21, s21
	v_rcp_f32_e32 v96, v96
	v_rcp_f32_e32 v97, v97
	v_rcp_f32_e32 v98, v98
	v_rcp_f32_e32 v99, v99
	v_rcp_f32_e32 v92, v92
	v_rcp_f32_e32 v93, v93
	v_rcp_f32_e32 v94, v94
	v_rcp_f32_e32 v95, v95
	v_rcp_f32_e32 v88, v88
	v_rcp_f32_e32 v89, v89
	v_rcp_f32_e32 v90, v90
	v_rcp_f32_e32 v91, v91
	v_rcp_f32_e32 v84, v84
	v_rcp_f32_e32 v85, v85
	v_rcp_f32_e32 v86, v86
	v_rcp_f32_e32 v87, v87
	v_cvt_rpi_i32_f32_e32 v96, v96
	v_cvt_rpi_i32_f32_e32 v88, v88
	v_cvt_rpi_i32_f32_sdwa v96, v97 dst_sel:BYTE_1 dst_unused:UNUSED_PRESERVE src0_sel:DWORD
	v_cvt_rpi_i32_f32_sdwa v88, v89 dst_sel:BYTE_1 dst_unused:UNUSED_PRESERVE src0_sel:DWORD
	v_cvt_rpi_i32_f32_e32 v97, v92
	v_cvt_rpi_i32_f32_e32 v89, v84
	v_cvt_rpi_i32_f32_sdwa v96, v98 dst_sel:BYTE_2 dst_unused:UNUSED_PRESERVE src0_sel:DWORD
	v_cvt_rpi_i32_f32_sdwa v88, v90 dst_sel:BYTE_2 dst_unused:UNUSED_PRESERVE src0_sel:DWORD
	v_cvt_rpi_i32_f32_sdwa v97, v93 dst_sel:BYTE_1 dst_unused:UNUSED_PRESERVE src0_sel:DWORD
	v_cvt_rpi_i32_f32_sdwa v89, v85 dst_sel:BYTE_1 dst_unused:UNUSED_PRESERVE src0_sel:DWORD
	v_cvt_rpi_i32_f32_sdwa v96, v99 dst_sel:BYTE_3 dst_unused:UNUSED_PRESERVE src0_sel:DWORD
	v_cvt_rpi_i32_f32_sdwa v88, v91 dst_sel:BYTE_3 dst_unused:UNUSED_PRESERVE src0_sel:DWORD
	v_cvt_rpi_i32_f32_sdwa v97, v94 dst_sel:BYTE_2 dst_unused:UNUSED_PRESERVE src0_sel:DWORD
	v_cvt_rpi_i32_f32_sdwa v89, v86 dst_sel:BYTE_2 dst_unused:UNUSED_PRESERVE src0_sel:DWORD
	v_cvt_rpi_i32_f32_sdwa v97, v95 dst_sel:BYTE_3 dst_unused:UNUSED_PRESERVE src0_sel:DWORD
	v_cvt_rpi_i32_f32_sdwa v89, v87 dst_sel:BYTE_3 dst_unused:UNUSED_PRESERVE src0_sel:DWORD
	ds_bpermute_b32 v96, v17, v96
	ds_bpermute_b32 v97, v17, v97
	ds_bpermute_b32 v88, v17, v88
	ds_bpermute_b32 v89, v17, v89
	s_waitcnt lgkmcnt(4)
	global_store_dwordx2 v[222:223], v[112:113], off
	global_store_dwordx2 v[224:225], v[104:105], off
	v_pk_fma_f32 v[80:81], v[80:81], s[20:21], v[214:215] op_sel_hi:[1,0,1]
	v_pk_fma_f32 v[82:83], v[82:83], s[20:21], v[216:217] op_sel_hi:[1,0,1]
	v_pk_fma_f32 v[76:77], v[76:77], s[20:21], v[218:219] op_sel_hi:[1,0,1]
	v_pk_fma_f32 v[78:79], v[78:79], s[20:21], v[220:221] op_sel_hi:[1,0,1]
	v_pk_fma_f32 v[72:73], v[72:73], s[20:21], v[214:215] op_sel_hi:[1,0,1]
	v_pk_fma_f32 v[74:75], v[74:75], s[20:21], v[216:217] op_sel_hi:[1,0,1]
	v_pk_fma_f32 v[68:69], v[68:69], s[20:21], v[218:219] op_sel_hi:[1,0,1]
	v_pk_fma_f32 v[70:71], v[70:71], s[20:21], v[220:221] op_sel_hi:[1,0,1]
	v_exp_f32_e32 v80, v80
	v_exp_f32_e32 v81, v81
	v_exp_f32_e32 v82, v82
	v_exp_f32_e32 v83, v83
	v_exp_f32_e32 v76, v76
	v_exp_f32_e32 v77, v77
	v_exp_f32_e32 v78, v78
	v_exp_f32_e32 v79, v79
	v_exp_f32_e32 v72, v72
	v_exp_f32_e32 v73, v73
	v_exp_f32_e32 v74, v74
	v_exp_f32_e32 v75, v75
	v_exp_f32_e32 v68, v68
	v_exp_f32_e32 v69, v69
	v_exp_f32_e32 v70, v70
	v_exp_f32_e32 v71, v71
	v_fma_f32 v80, v80, s21, s21
	v_fma_f32 v81, v81, s21, s21
	v_fma_f32 v82, v82, s21, s21
	v_fma_f32 v83, v83, s21, s21
	v_fma_f32 v76, v76, s21, s21
	v_fma_f32 v77, v77, s21, s21
	v_fma_f32 v78, v78, s21, s21
	v_fma_f32 v79, v79, s21, s21
	v_fma_f32 v72, v72, s21, s21
	v_fma_f32 v73, v73, s21, s21
	v_fma_f32 v74, v74, s21, s21
	v_fma_f32 v75, v75, s21, s21
	v_fma_f32 v68, v68, s21, s21
	v_fma_f32 v69, v69, s21, s21
	v_fma_f32 v70, v70, s21, s21
	v_fma_f32 v71, v71, s21, s21
	v_rcp_f32_e32 v80, v80
	v_rcp_f32_e32 v81, v81
	v_rcp_f32_e32 v82, v82
	v_rcp_f32_e32 v83, v83
	v_rcp_f32_e32 v76, v76
	v_rcp_f32_e32 v77, v77
	v_rcp_f32_e32 v78, v78
	v_rcp_f32_e32 v79, v79
	v_rcp_f32_e32 v72, v72
	v_rcp_f32_e32 v73, v73
	v_rcp_f32_e32 v74, v74
	v_rcp_f32_e32 v75, v75
	v_rcp_f32_e32 v68, v68
	v_rcp_f32_e32 v69, v69
	v_rcp_f32_e32 v70, v70
	v_rcp_f32_e32 v71, v71
	v_cvt_rpi_i32_f32_e32 v80, v80
	v_cvt_rpi_i32_f32_e32 v72, v72
	v_cvt_rpi_i32_f32_sdwa v80, v81 dst_sel:BYTE_1 dst_unused:UNUSED_PRESERVE src0_sel:DWORD
	v_cvt_rpi_i32_f32_sdwa v72, v73 dst_sel:BYTE_1 dst_unused:UNUSED_PRESERVE src0_sel:DWORD
	v_cvt_rpi_i32_f32_e32 v81, v76
	v_cvt_rpi_i32_f32_e32 v73, v68
	v_cvt_rpi_i32_f32_sdwa v80, v82 dst_sel:BYTE_2 dst_unused:UNUSED_PRESERVE src0_sel:DWORD
	v_cvt_rpi_i32_f32_sdwa v72, v74 dst_sel:BYTE_2 dst_unused:UNUSED_PRESERVE src0_sel:DWORD
	v_cvt_rpi_i32_f32_sdwa v81, v77 dst_sel:BYTE_1 dst_unused:UNUSED_PRESERVE src0_sel:DWORD
	v_cvt_rpi_i32_f32_sdwa v73, v69 dst_sel:BYTE_1 dst_unused:UNUSED_PRESERVE src0_sel:DWORD
	v_cvt_rpi_i32_f32_sdwa v80, v83 dst_sel:BYTE_3 dst_unused:UNUSED_PRESERVE src0_sel:DWORD
	v_cvt_rpi_i32_f32_sdwa v72, v75 dst_sel:BYTE_3 dst_unused:UNUSED_PRESERVE src0_sel:DWORD
	v_cvt_rpi_i32_f32_sdwa v81, v78 dst_sel:BYTE_2 dst_unused:UNUSED_PRESERVE src0_sel:DWORD
	v_cvt_rpi_i32_f32_sdwa v73, v70 dst_sel:BYTE_2 dst_unused:UNUSED_PRESERVE src0_sel:DWORD
	v_cvt_rpi_i32_f32_sdwa v81, v79 dst_sel:BYTE_3 dst_unused:UNUSED_PRESERVE src0_sel:DWORD
	v_cvt_rpi_i32_f32_sdwa v73, v71 dst_sel:BYTE_3 dst_unused:UNUSED_PRESERVE src0_sel:DWORD
	ds_bpermute_b32 v80, v17, v80
	ds_bpermute_b32 v81, v17, v81
	ds_bpermute_b32 v72, v17, v72
	ds_bpermute_b32 v73, v17, v73
	s_waitcnt lgkmcnt(4)
; __device__ __forceinline__ float fast_sigmoid(float z) { return __builtin_amdgcn_rcpf(1.f + __builtin_amdgcn_exp2f(-z * LOG2E)); }
;     static __device__ __forceinline__ unsigned q8(float z) { return (unsigned)(fast_sigmoid(z) * 255.f + 0.5f); }
;     __device__ __forceinline__ void operator()(const f32x4 (&acc)[2][2][4][2], const g8::Unit& u, int wr, int wc, int fr, int fq) const {
;         const int row0 = u.pm * 256 + wr * 64 + fr, col0 = u.pn * 256 + wc * 32 + 8 * fq;
; #pragma unroll
;         for (int bj = 0; bj < 2; ++bj) {
;             const f32x4 bv0 = *(const f32x4*)(bgate + col0 + bj * 128), bv1 = *(const f32x4*)(bgate + col0 + bj * 128 + 4);
; #pragma unroll
;             for (int ai = 0; ai < 2; ++ai)
; #pragma unroll
;                 for (int m = 0; m < 4; ++m) { const int row = row0 + ai * 128 + m * 16; unsigned char* rp = GT + (size_t)row * 4096 + col0 + bj * 128;
;                     const f32x4 v0 = acc[ai][bj][m][0] * 0.03125f + bv0, v1 = acc[ai][bj][m][1] * 0.03125f + bv1;
;                     u32x2 w; w.x = q8(v0[0]) | (q8(v0[1]) << 8) | (q8(v0[2]) << 16) | (q8(v0[3]) << 24); w.y = q8(v1[0]) | (q8(v1[1]) << 8) | (q8(v1[2]) << 16) | (q8(v1[3]) << 24);
;                     *(u32x2*)rp = w; } }
	global_store_dwordx2 v[226:227], v[96:97], off
	global_store_dwordx2 v[228:229], v[88:89], off
	v_pk_fma_f32 v[64:65], v[64:65], s[20:21], v[214:215] op_sel_hi:[1,0,1]
	v_pk_fma_f32 v[66:67], v[66:67], s[20:21], v[216:217] op_sel_hi:[1,0,1]
	v_pk_fma_f32 v[60:61], v[60:61], s[20:21], v[218:219] op_sel_hi:[1,0,1]
	v_pk_fma_f32 v[62:63], v[62:63], s[20:21], v[220:221] op_sel_hi:[1,0,1]
	v_pk_fma_f32 v[56:57], v[56:57], s[20:21], v[214:215] op_sel_hi:[1,0,1]
	v_pk_fma_f32 v[58:59], v[58:59], s[20:21], v[216:217] op_sel_hi:[1,0,1]
	v_pk_fma_f32 v[52:53], v[52:53], s[20:21], v[218:219] op_sel_hi:[1,0,1]
	v_pk_fma_f32 v[54:55], v[54:55], s[20:21], v[220:221] op_sel_hi:[1,0,1]
	v_exp_f32_e32 v64, v64
	v_exp_f32_e32 v65, v65
	v_exp_f32_e32 v66, v66
	v_exp_f32_e32 v67, v67
	v_exp_f32_e32 v60, v60
	v_exp_f32_e32 v61, v61
	v_exp_f32_e32 v62, v62
	v_exp_f32_e32 v63, v63
	v_exp_f32_e32 v56, v56
	v_exp_f32_e32 v57, v57
	v_exp_f32_e32 v58, v58
	v_exp_f32_e32 v59, v59
	v_exp_f32_e32 v52, v52
	v_exp_f32_e32 v53, v53
	v_exp_f32_e32 v54, v54
	v_exp_f32_e32 v55, v55
	v_fma_f32 v64, v64, s21, s21
	v_fma_f32 v65, v65, s21, s21
	v_fma_f32 v66, v66, s21, s21
	v_fma_f32 v67, v67, s21, s21
	v_fma_f32 v60, v60, s21, s21
	v_fma_f32 v61, v61, s21, s21
	v_fma_f32 v62, v62, s21, s21
	v_fma_f32 v63, v63, s21, s21
	v_fma_f32 v56, v56, s21, s21
	v_fma_f32 v57, v57, s21, s21
	v_fma_f32 v58, v58, s21, s21
	v_fma_f32 v59, v59, s21, s21
	v_fma_f32 v52, v52, s21, s21
	v_fma_f32 v53, v53, s21, s21
	v_fma_f32 v54, v54, s21, s21
	v_fma_f32 v55, v55, s21, s21
	v_rcp_f32_e32 v64, v64
	v_rcp_f32_e32 v65, v65
	v_rcp_f32_e32 v66, v66
	v_rcp_f32_e32 v67, v67
	v_rcp_f32_e32 v60, v60
	v_rcp_f32_e32 v61, v61
	v_rcp_f32_e32 v62, v62
	v_rcp_f32_e32 v63, v63
	v_rcp_f32_e32 v56, v56
	v_rcp_f32_e32 v57, v57
	v_rcp_f32_e32 v58, v58
	v_rcp_f32_e32 v59, v59
	v_rcp_f32_e32 v52, v52
	v_rcp_f32_e32 v53, v53
	v_rcp_f32_e32 v54, v54
	v_rcp_f32_e32 v55, v55
	v_cvt_rpi_i32_f32_e32 v64, v64
	v_cvt_rpi_i32_f32_e32 v56, v56
	v_cvt_rpi_i32_f32_sdwa v64, v65 dst_sel:BYTE_1 dst_unused:UNUSED_PRESERVE src0_sel:DWORD
	v_cvt_rpi_i32_f32_sdwa v56, v57 dst_sel:BYTE_1 dst_unused:UNUSED_PRESERVE src0_sel:DWORD
	v_cvt_rpi_i32_f32_e32 v65, v60
	v_cvt_rpi_i32_f32_e32 v57, v52
	v_cvt_rpi_i32_f32_sdwa v64, v66 dst_sel:BYTE_2 dst_unused:UNUSED_PRESERVE src0_sel:DWORD
	v_cvt_rpi_i32_f32_sdwa v56, v58 dst_sel:BYTE_2 dst_unused:UNUSED_PRESERVE src0_sel:DWORD
	v_cvt_rpi_i32_f32_sdwa v65, v61 dst_sel:BYTE_1 dst_unused:UNUSED_PRESERVE src0_sel:DWORD
	v_cvt_rpi_i32_f32_sdwa v57, v53 dst_sel:BYTE_1 dst_unused:UNUSED_PRESERVE src0_sel:DWORD
	v_cvt_rpi_i32_f32_sdwa v64, v67 dst_sel:BYTE_3 dst_unused:UNUSED_PRESERVE src0_sel:DWORD
	v_cvt_rpi_i32_f32_sdwa v56, v59 dst_sel:BYTE_3 dst_unused:UNUSED_PRESERVE src0_sel:DWORD
	v_cvt_rpi_i32_f32_sdwa v65, v62 dst_sel:BYTE_2 dst_unused:UNUSED_PRESERVE src0_sel:DWORD
	v_cvt_rpi_i32_f32_sdwa v57, v54 dst_sel:BYTE_2 dst_unused:UNUSED_PRESERVE src0_sel:DWORD
	v_cvt_rpi_i32_f32_sdwa v65, v63 dst_sel:BYTE_3 dst_unused:UNUSED_PRESERVE src0_sel:DWORD
	v_cvt_rpi_i32_f32_sdwa v57, v55 dst_sel:BYTE_3 dst_unused:UNUSED_PRESERVE src0_sel:DWORD
	ds_bpermute_b32 v64, v17, v64
	ds_bpermute_b32 v65, v17, v65
	ds_bpermute_b32 v56, v17, v56
	ds_bpermute_b32 v57, v17, v57
	s_waitcnt lgkmcnt(4)
	global_store_dwordx2 v[8:9], v[80:81], off offset:128
	global_store_dwordx2 v[10:11], v[72:73], off offset:128
	v_pk_fma_f32 v[48:49], v[48:49], s[20:21], v[214:215] op_sel_hi:[1,0,1]
	v_pk_fma_f32 v[50:51], v[50:51], s[20:21], v[216:217] op_sel_hi:[1,0,1]
	v_pk_fma_f32 v[44:45], v[44:45], s[20:21], v[218:219] op_sel_hi:[1,0,1]
	v_pk_fma_f32 v[46:47], v[46:47], s[20:21], v[220:221] op_sel_hi:[1,0,1]
	v_pk_fma_f32 v[40:41], v[40:41], s[20:21], v[214:215] op_sel_hi:[1,0,1]
	v_pk_fma_f32 v[42:43], v[42:43], s[20:21], v[216:217] op_sel_hi:[1,0,1]
	v_pk_fma_f32 v[36:37], v[36:37], s[20:21], v[218:219] op_sel_hi:[1,0,1]
	v_pk_fma_f32 v[38:39], v[38:39], s[20:21], v[220:221] op_sel_hi:[1,0,1]
	v_exp_f32_e32 v48, v48
	v_exp_f32_e32 v49, v49
	v_exp_f32_e32 v50, v50
	v_exp_f32_e32 v51, v51
	v_exp_f32_e32 v44, v44
	v_exp_f32_e32 v45, v45
	v_exp_f32_e32 v46, v46
	v_exp_f32_e32 v47, v47
	v_exp_f32_e32 v40, v40
	v_exp_f32_e32 v41, v41
	v_exp_f32_e32 v42, v42
	v_exp_f32_e32 v43, v43
	v_exp_f32_e32 v36, v36
	v_exp_f32_e32 v37, v37
	v_exp_f32_e32 v38, v38
	v_exp_f32_e32 v39, v39
	v_fma_f32 v48, v48, s21, s21
	v_fma_f32 v49, v49, s21, s21
	v_fma_f32 v50, v50, s21, s21
	v_fma_f32 v51, v51, s21, s21
	v_fma_f32 v44, v44, s21, s21
	v_fma_f32 v45, v45, s21, s21
	v_fma_f32 v46, v46, s21, s21
	v_fma_f32 v47, v47, s21, s21
	v_fma_f32 v40, v40, s21, s21
	v_fma_f32 v41, v41, s21, s21
	v_fma_f32 v42, v42, s21, s21
	v_fma_f32 v43, v43, s21, s21
	v_fma_f32 v36, v36, s21, s21
	v_fma_f32 v37, v37, s21, s21
	v_fma_f32 v38, v38, s21, s21
	v_fma_f32 v39, v39, s21, s21
	v_rcp_f32_e32 v48, v48
	v_rcp_f32_e32 v49, v49
	v_rcp_f32_e32 v50, v50
	v_rcp_f32_e32 v51, v51
	v_rcp_f32_e32 v44, v44
	v_rcp_f32_e32 v45, v45
	v_rcp_f32_e32 v46, v46
	v_rcp_f32_e32 v47, v47
	v_rcp_f32_e32 v40, v40
	v_rcp_f32_e32 v41, v41
	v_rcp_f32_e32 v42, v42
	v_rcp_f32_e32 v43, v43
	v_rcp_f32_e32 v36, v36
	v_rcp_f32_e32 v37, v37
	v_rcp_f32_e32 v38, v38
	v_rcp_f32_e32 v39, v39
	v_cvt_rpi_i32_f32_e32 v48, v48
	v_cvt_rpi_i32_f32_e32 v40, v40
	v_cvt_rpi_i32_f32_sdwa v48, v49 dst_sel:BYTE_1 dst_unused:UNUSED_PRESERVE src0_sel:DWORD
	v_cvt_rpi_i32_f32_sdwa v40, v41 dst_sel:BYTE_1 dst_unused:UNUSED_PRESERVE src0_sel:DWORD
	v_cvt_rpi_i32_f32_e32 v49, v44
	v_cvt_rpi_i32_f32_e32 v41, v36
	v_cvt_rpi_i32_f32_sdwa v48, v50 dst_sel:BYTE_2 dst_unused:UNUSED_PRESERVE src0_sel:DWORD
	v_cvt_rpi_i32_f32_sdwa v40, v42 dst_sel:BYTE_2 dst_unused:UNUSED_PRESERVE src0_sel:DWORD
	v_cvt_rpi_i32_f32_sdwa v49, v45 dst_sel:BYTE_1 dst_unused:UNUSED_PRESERVE src0_sel:DWORD
	v_cvt_rpi_i32_f32_sdwa v41, v37 dst_sel:BYTE_1 dst_unused:UNUSED_PRESERVE src0_sel:DWORD
	v_cvt_rpi_i32_f32_sdwa v48, v51 dst_sel:BYTE_3 dst_unused:UNUSED_PRESERVE src0_sel:DWORD
	v_cvt_rpi_i32_f32_sdwa v40, v43 dst_sel:BYTE_3 dst_unused:UNUSED_PRESERVE src0_sel:DWORD
	v_cvt_rpi_i32_f32_sdwa v49, v46 dst_sel:BYTE_2 dst_unused:UNUSED_PRESERVE src0_sel:DWORD
	v_cvt_rpi_i32_f32_sdwa v41, v38 dst_sel:BYTE_2 dst_unused:UNUSED_PRESERVE src0_sel:DWORD
	v_cvt_rpi_i32_f32_sdwa v49, v47 dst_sel:BYTE_3 dst_unused:UNUSED_PRESERVE src0_sel:DWORD
	v_cvt_rpi_i32_f32_sdwa v41, v39 dst_sel:BYTE_3 dst_unused:UNUSED_PRESERVE src0_sel:DWORD
	ds_bpermute_b32 v48, v17, v48
	ds_bpermute_b32 v49, v17, v49
	ds_bpermute_b32 v40, v17, v40
	ds_bpermute_b32 v41, v17, v41
	s_waitcnt lgkmcnt(4)
; __device__ __forceinline__ float fast_sigmoid(float z) { return __builtin_amdgcn_rcpf(1.f + __builtin_amdgcn_exp2f(-z * LOG2E)); }
;     static __device__ __forceinline__ unsigned q8(float z) { return (unsigned)(fast_sigmoid(z) * 255.f + 0.5f); }
;     __device__ __forceinline__ void operator()(const f32x4 (&acc)[2][2][4][2], const g8::Unit& u, int wr, int wc, int fr, int fq) const {
;         const int row0 = u.pm * 256 + wr * 64 + fr, col0 = u.pn * 256 + wc * 32 + 8 * fq;
; #pragma unroll
;         for (int bj = 0; bj < 2; ++bj) {
;             const f32x4 bv0 = *(const f32x4*)(bgate + col0 + bj * 128), bv1 = *(const f32x4*)(bgate + col0 + bj * 128 + 4);
; #pragma unroll
;             for (int ai = 0; ai < 2; ++ai)
; #pragma unroll
;                 for (int m = 0; m < 4; ++m) { const int row = row0 + ai * 128 + m * 16; unsigned char* rp = GT + (size_t)row * 4096 + col0 + bj * 128;
;                     const f32x4 v0 = acc[ai][bj][m][0] * 0.03125f + bv0, v1 = acc[ai][bj][m][1] * 0.03125f + bv1;
;                     u32x2 w; w.x = q8(v0[0]) | (q8(v0[1]) << 8) | (q8(v0[2]) << 16) | (q8(v0[3]) << 24); w.y = q8(v1[0]) | (q8(v1[1]) << 8) | (q8(v1[2]) << 16) | (q8(v1[3]) << 24);
;                     *(u32x2*)rp = w; } }
	global_store_dwordx2 v[14:15], v[64:65], off offset:128
	global_store_dwordx2 v[168:169], v[56:57], off offset:128
	v_pk_fma_f32 v[32:33], v[32:33], s[20:21], v[214:215] op_sel_hi:[1,0,1]
	v_pk_fma_f32 v[34:35], v[34:35], s[20:21], v[216:217] op_sel_hi:[1,0,1]
	v_pk_fma_f32 v[26:27], v[26:27], s[20:21], v[218:219] op_sel_hi:[1,0,1]
	v_pk_fma_f32 v[28:29], v[28:29], s[20:21], v[220:221] op_sel_hi:[1,0,1]
	v_pk_fma_f32 v[22:23], v[22:23], s[20:21], v[214:215] op_sel_hi:[1,0,1]
	v_pk_fma_f32 v[24:25], v[24:25], s[20:21], v[216:217] op_sel_hi:[1,0,1]
	v_pk_fma_f32 v[18:19], v[18:19], s[20:21], v[218:219] op_sel_hi:[1,0,1]
	v_pk_fma_f32 v[20:21], v[20:21], s[20:21], v[220:221] op_sel_hi:[1,0,1]
	v_exp_f32_e32 v32, v32
	v_exp_f32_e32 v33, v33
	v_exp_f32_e32 v34, v34
	v_exp_f32_e32 v35, v35
	v_exp_f32_e32 v26, v26
	v_exp_f32_e32 v27, v27
	v_exp_f32_e32 v28, v28
	v_exp_f32_e32 v29, v29
	v_exp_f32_e32 v22, v22
	v_exp_f32_e32 v23, v23
	v_exp_f32_e32 v24, v24
	v_exp_f32_e32 v25, v25
	v_exp_f32_e32 v18, v18
	v_exp_f32_e32 v19, v19
	v_exp_f32_e32 v20, v20
	v_exp_f32_e32 v21, v21
	v_fma_f32 v32, v32, s21, s21
	v_fma_f32 v33, v33, s21, s21
	v_fma_f32 v34, v34, s21, s21
	v_fma_f32 v35, v35, s21, s21
	v_fma_f32 v26, v26, s21, s21
	v_fma_f32 v27, v27, s21, s21
	v_fma_f32 v28, v28, s21, s21
	v_fma_f32 v29, v29, s21, s21
	v_fma_f32 v22, v22, s21, s21
	v_fma_f32 v23, v23, s21, s21
	v_fma_f32 v24, v24, s21, s21
	v_fma_f32 v25, v25, s21, s21
	v_fma_f32 v18, v18, s21, s21
	v_fma_f32 v19, v19, s21, s21
	v_fma_f32 v20, v20, s21, s21
	v_fma_f32 v21, v21, s21, s21
	v_rcp_f32_e32 v32, v32
	v_rcp_f32_e32 v33, v33
	v_rcp_f32_e32 v34, v34
	v_rcp_f32_e32 v35, v35
	v_rcp_f32_e32 v26, v26
	v_rcp_f32_e32 v27, v27
	v_rcp_f32_e32 v28, v28
	v_rcp_f32_e32 v29, v29
	v_rcp_f32_e32 v22, v22
	v_rcp_f32_e32 v23, v23
	v_rcp_f32_e32 v24, v24
	v_rcp_f32_e32 v25, v25
	v_rcp_f32_e32 v18, v18
	v_rcp_f32_e32 v19, v19
	v_rcp_f32_e32 v20, v20
	v_rcp_f32_e32 v21, v21
	v_cvt_rpi_i32_f32_e32 v32, v32
	v_cvt_rpi_i32_f32_e32 v22, v22
	v_cvt_rpi_i32_f32_sdwa v32, v33 dst_sel:BYTE_1 dst_unused:UNUSED_PRESERVE src0_sel:DWORD
	v_cvt_rpi_i32_f32_sdwa v22, v23 dst_sel:BYTE_1 dst_unused:UNUSED_PRESERVE src0_sel:DWORD
	v_cvt_rpi_i32_f32_e32 v33, v26
	v_cvt_rpi_i32_f32_e32 v23, v18
	v_cvt_rpi_i32_f32_sdwa v32, v34 dst_sel:BYTE_2 dst_unused:UNUSED_PRESERVE src0_sel:DWORD
	v_cvt_rpi_i32_f32_sdwa v22, v24 dst_sel:BYTE_2 dst_unused:UNUSED_PRESERVE src0_sel:DWORD
	v_cvt_rpi_i32_f32_sdwa v33, v27 dst_sel:BYTE_1 dst_unused:UNUSED_PRESERVE src0_sel:DWORD
	v_cvt_rpi_i32_f32_sdwa v23, v19 dst_sel:BYTE_1 dst_unused:UNUSED_PRESERVE src0_sel:DWORD
	v_cvt_rpi_i32_f32_sdwa v32, v35 dst_sel:BYTE_3 dst_unused:UNUSED_PRESERVE src0_sel:DWORD
	v_cvt_rpi_i32_f32_sdwa v22, v25 dst_sel:BYTE_3 dst_unused:UNUSED_PRESERVE src0_sel:DWORD
	v_cvt_rpi_i32_f32_sdwa v33, v28 dst_sel:BYTE_2 dst_unused:UNUSED_PRESERVE src0_sel:DWORD
	v_cvt_rpi_i32_f32_sdwa v23, v20 dst_sel:BYTE_2 dst_unused:UNUSED_PRESERVE src0_sel:DWORD
	v_cvt_rpi_i32_f32_sdwa v33, v29 dst_sel:BYTE_3 dst_unused:UNUSED_PRESERVE src0_sel:DWORD
	v_cvt_rpi_i32_f32_sdwa v23, v21 dst_sel:BYTE_3 dst_unused:UNUSED_PRESERVE src0_sel:DWORD
	ds_bpermute_b32 v32, v17, v32
	ds_bpermute_b32 v33, v17, v33
	ds_bpermute_b32 v22, v17, v22
	ds_bpermute_b32 v23, v17, v23
	s_waitcnt lgkmcnt(4)
	global_store_dwordx2 v[222:223], v[48:49], off offset:128
	global_store_dwordx2 v[224:225], v[40:41], off offset:128
	s_waitcnt lgkmcnt(0)
	global_store_dwordx2 v[226:227], v[32:33], off offset:128
	global_store_dwordx2 v[228:229], v[22:23], off offset:128
	s_mov_b64 s[44:45], -1
	s_andn2_b64 vcc, exec, s[14:15]
	s_cbranch_vccnz .LBB0_447
	s_and_b64 vcc, exec, s[38:39]
	s_cbranch_vccnz .LBB0_446
	s_barrier
	s_branch .LBB0_446

; #define LAS __attribute__((address_space(3)))
; __device__ __forceinline__ KA kargs() { KA p = (KA)__builtin_amdgcn_kernarg_segment_ptr(); asm volatile("" : "+s"(p)); return p; }
; template <int lda, int ldb, class Epi, class Sched>
; __device__ __forceinline__ void gemm_phase(LAS unsigned char* lds, int wid, int lane, const char* baseA, const char* baseB, const Sched& S, const Epi& E) {
;     const int tid = wid * 64 + lane, wr = wid >> 2, wc = wid & 3, fr = lane & 15, fq = lane >> 4;
;     unsigned voffA[2], voffB[2]; int gR[2], gC[2];
; #pragma unroll
;     for (int i = 0; i < 2; ++i) { int R, C; stage_rc(tid * 16 + i * 8192, R, C); const int Rb = Epi::PERM ? ((R & ~31) + perm32(R & 31)) : R;
;         voffA[i] = (unsigned)(R * lda + C) * 2u; voffB[i] = (unsigned)(Rb * ldb + C) * 2u; gR[i] = R; gC[i] = C; }
;     unsigned goff[2][2], gnxt[2][2];
;     ...
;     const size_t kstep = (size_t)(BK * 2);
;     const size_t hstepA = (size_t)HALF * lda * 2, hstepB = (size_t)HALF * ldb * 2;
;     const unsigned ldsw = (unsigned)wid * 1024u;
;     const int aoff = lds_byte(wr * 64 + fr, fq * 8), boff = lds_byte(wc * 32 + fr, fq * 8);
; __device__ __forceinline__ void gate_batches(LAS unsigned char* lds, int wv, int l, int max_batches) {
;     const Frame F = make_frame(lds, wv); const KA a = kargs();
;     unsigned* qg = F.ctl + CW_CVQ + l * 16 + 8;
;     volatile LAS int* gslot = (volatile LAS int*)(lds + MISC_OFF + 512);
; #pragma unroll 1
;     for (int nb = 0; nb < max_batches; ++nb) {
;         int bt;
;         if (F.tid == 0) *gslot = (int)__hip_atomic_fetch_add(qg, 1u, __ATOMIC_RELAXED, __HIP_MEMORY_SCOPE_AGENT);
.LBB0_1068:
	v_readlane_b32 s42, v253, 0
	v_readlane_b32 s43, v253, 1
	s_mov_b64 s[2:3], s[42:43]
	s_load_dwordx2 s[14:15], s[2:3], 0xf0
	s_mov_b32 s2, -1
	v_mov_b32_e32 v17, 1
	v_mbcnt_lo_u32_b32 v0, s2, 0
	v_mbcnt_hi_u32_b32 v0, s2, v0
	v_readlane_b32 s2, v255, 7
	v_readlane_b32 s3, v255, 8
	s_waitcnt lgkmcnt(0)
	s_add_u32 s2, s14, s2
	s_addc_u32 s3, s15, s3
	s_add_u32 s44, s2, 0x2e20
	s_addc_u32 s45, s3, 0
	s_add_u32 s46, s14, 0x16900000
	s_addc_u32 s47, s15, 0
	s_lshl_b32 s10, s72, 12
	v_readlane_b32 s2, v253, 8
	s_ashr_i32 s11, s10, 31
	s_mov_b32 s3, 0xbd00000
	v_cmp_eq_u32_e64 s[38:39], s2, v0
	s_add_u32 s2, s14, 0xad00000
	s_addc_u32 s13, s15, 0
	s_bitcmp0_b32 s72, 0
	s_cselect_b64 s[6:7], -1, 0
	s_and_b64 s[16:17], s[6:7], exec
	v_and_b32_e32 v1, 15, v0
	s_cselect_b32 s3, s3, 0x22900000
	v_or_b32_e32 v2, s9, v1
	s_add_u32 s31, s14, s3
	v_lshlrev_b32_e32 v4, 6, v2
	v_and_b32_e32 v5, 48, v0
	s_movk_i32 s3, 0x3c0
	v_lshrrev_b32_e32 v3, 6, v0
	v_and_or_b32 v4, v4, s3, v5
	v_lshl_or_b32 v1, v1, 6, v5
	v_lshlrev_b32_e32 v5, 2, v0
	v_lshl_add_u32 v0, v0, 4, s27
	v_add_u32_e32 v7, 0x2000, v0
	v_ashrrev_i32_e32 v8, 31, v7
	v_lshrrev_b32_e32 v8, 22, v8
	v_add_u32_e32 v8, v7, v8
	v_ashrrev_i32_e32 v8, 10, v8
	v_mul_i32_i24_e32 v9, 0x400, v8
	v_sub_u32_e32 v7, v7, v9
	v_lshrrev_b32_e32 v9, 4, v7
	v_bitop3_b32 v7, v9, v7, 32 bitop3:0x6c
	v_ashrrev_i32_e32 v9, 31, v7
	v_lshrrev_b32_e32 v9, 26, v9
	v_add_u32_e32 v9, v7, v9
	v_ashrrev_i32_e32 v10, 6, v9
	v_lshlrev_b32_e32 v11, 3, v8
	v_and_b32_e32 v9, 0xffc0, v9
	v_and_b32_e32 v11, -16, v11
	v_sub_u32_e32 v7, v7, v9
	v_readlane_b32 s3, v254, 8
	v_add_u32_e32 v11, v10, v11
	v_lshrrev_b16_e32 v9, 7, v7
	v_lshlrev_b32_e32 v6, 10, v3
	v_add_lshl_u32 v3, v3, s3, 10
	v_and_b32_e32 v12, 3, v10
	s_mov_b32 s3, 0x3fffe0
	v_lshrrev_b32_e32 v13, 2, v11
	v_lshlrev_b32_e32 v14, 1, v11
	v_and_b32_e32 v9, 1, v9
	v_and_or_b32 v12, v11, s3, v12
	v_and_b32_e32 v13, 4, v13
	v_and_b32_e32 v14, 24, v14
	v_add_u16_e32 v7, v7, v9
	v_or3_b32 v12, v12, v13, v14
	v_lshlrev_b32_e32 v13, 5, v8
	v_ashrrev_i16_sdwa v7, v17, sext(v7) dst_sel:DWORD dst_unused:UNUSED_PAD src0_sel:DWORD src1_sel:BYTE_0
	v_and_b32_e32 v13, 32, v13
	v_bfe_i32 v7, v7, 0, 16
	v_add_lshl_u32 v9, v13, v7, 1
	v_lshl_add_u32 v156, v12, 10, v9
	v_lshl_add_u32 v158, v11, 10, v9
	v_ashrrev_i32_e32 v9, 31, v0
	v_lshrrev_b32_e32 v9, 22, v9
	v_add_u32_e32 v9, v0, v9
	v_ashrrev_i32_e32 v9, 10, v9
	v_mul_i32_i24_e32 v11, 0x400, v9
	v_sub_u32_e32 v0, v0, v11
	v_lshrrev_b32_e32 v11, 4, v0
	v_bitop3_b32 v0, v11, v0, 32 bitop3:0x6c
	v_and_b32_e32 v5, 32, v5
	v_ashrrev_i32_e32 v11, 31, v0
	v_lshrrev_b32_e32 v11, 26, v11
	v_bitop3_b32 v1, v1, v3, v5 bitop3:0xde
	v_add_u32_e32 v11, v0, v11
	v_lshlrev_b32_e32 v13, 3, v9
	v_add_u32_e32 v30, 0x10000, v1
	v_add_u32_e32 v148, 0x14000, v1
	v_add_u32_e32 v151, 0x18000, v1
	v_add_u32_e32 v176, 0x1c000, v1
	v_add_u32_e32 v177, 0x10400, v1
	v_add_u32_e32 v178, 0x10800, v1
	v_add_u32_e32 v179, 0x10c00, v1
	v_add_u32_e32 v180, 0x14400, v1
	v_add_u32_e32 v181, 0x14800, v1
	v_add_u32_e32 v205, 0x14c00, v1
	v_add_u32_e32 v206, 0x18400, v1
	v_add_u32_e32 v207, 0x18800, v1
	v_add_u32_e32 v208, 0x18c00, v1
	v_add_u32_e32 v209, 0x1c400, v1
	v_add_u32_e32 v210, 0x1c800, v1
	v_add_u32_e32 v211, 0x1cc00, v1
	v_lshlrev_b32_e32 v1, 13, v8
	v_ashrrev_i32_e32 v12, 6, v11
	v_and_b32_e32 v13, -16, v13
	v_and_b32_e32 v1, 0xffffc000, v1
	v_add_u32_e32 v13, v12, v13
	v_lshl_add_u32 v1, v10, 10, v1
	v_lshlrev_b32_e32 v3, 6, v8
	v_and_b32_e32 v14, 3, v12
	v_lshrrev_b32_e32 v15, 2, v13
	v_lshlrev_b32_e32 v16, 1, v13
	v_and_b32_e32 v11, 0xc0, v11
	v_and_or_b32 v1, v3, 64, v1
	v_and_or_b32 v14, v13, s3, v14
	v_and_b32_e32 v15, 4, v15
	v_and_b32_e32 v16, 24, v16
	v_sub_u32_e32 v0, v0, v11
	v_lshl_add_u32 v164, v7, 1, v1
	v_lshlrev_b32_e32 v1, 13, v9
	v_lshlrev_b32_e32 v2, 2, v2
	v_or3_b32 v14, v14, v15, v16
	v_lshlrev_b32_e32 v15, 5, v9
	v_ashrrev_i16_sdwa v0, v17, sext(v0) dst_sel:DWORD dst_unused:UNUSED_PAD src0_sel:DWORD src1_sel:BYTE_0
	v_and_b32_e32 v1, 0xffffc000, v1
	v_and_b32_e32 v2, 32, v2
	v_and_b32_e32 v15, 32, v15
	v_bfe_i32 v0, v0, 0, 16
	v_lshl_add_u32 v1, v12, 10, v1
	v_lshlrev_b32_e32 v3, 6, v9
	v_add_lshl_u32 v11, v15, v0, 1
	v_bitop3_b32 v2, v4, v6, v2 bitop3:0xde
	v_and_or_b32 v1, v3, 64, v1
	v_readlane_b32 s3, v253, 61
	s_mov_b32 s1, 0
	s_addc_u32 s58, s15, 0
	v_mov_b32_e32 v251, 1
	v_lshl_add_u32 v160, v14, 10, v11
	v_lshl_add_u32 v162, v13, 10, v11
	v_mov_b32_e32 v161, v31
	v_mov_b32_e32 v157, v31
	v_mov_b32_e32 v163, v31
	v_mov_b32_e32 v159, v31
	v_mov_b32_e32 v165, v31
	v_lshl_add_u32 v166, v0, 1, v1
	v_mov_b32_e32 v167, v31
	s_lshl_b64 s[48:49], s[10:11], 2
	v_add_u32_e32 v212, s3, v2
	s_and_saveexec_b64 s[10:11], s[38:39]
	v_mov_b32_e32 v150, 1
	global_atomic_add v150, v31, v150, s[44:45] sc0
	s_or_b64 exec, exec, s[10:11]
	s_branch .LBB0_1071

; __device__ __forceinline__ void gate_batches(LAS unsigned char* lds, int wv, int l, int max_batches) {
;     ...
;     for (int nb = 0; nb < max_batches; ++nb) {
;         int bt;
;         if (F.tid == 0) *gslot = (int)__hip_atomic_fetch_add(qg, 1u, __ATOMIC_RELAXED, __HIP_MEMORY_SCOPE_AGENT);
;         __syncthreads(); bt = *gslot; __syncthreads();
.LBB0_1071:
	s_and_saveexec_b64 s[10:11], s[38:39]
	s_cbranch_execz .LBB0_1075
	s_mov_b64 s[16:17], exec
	v_mbcnt_lo_u32_b32 v0, s16, 0
	v_mbcnt_hi_u32_b32 v0, s17, v0
	v_cmp_eq_u32_e32 vcc, 0, v0
	s_and_saveexec_b64 s[14:15], vcc
	s_cbranch_execz .LBB0_1074
	s_waitcnt vmcnt(0)
	v_mov_b32_e32 v1, v150

;     __device__ bool next(int i, Unit& u) const { int pm, pn; if (!T.tile(i, pm, pn)) return false; u.ao = (unsigned)pm * (unsigned)(BM * LDA * 2); u.bo = (unsigned)pn * (unsigned)(BM * LDB * 2); u.nt = K / BK; u.pm = pm; u.pn = pn; u.tag = 0; return true; }
;     __device__ bool next(int i, Unit& u) const { int pm, pn; if (!T.tile(i, pm, pn)) return false; u.ao = (unsigned)pm * (unsigned)(BM * LDA * 2); u.bo = (unsigned)pn * (unsigned)(128 * LDB * 2); u.nt = K / BK; u.pm = pm; u.pn = pn; u.tag = 0; return true; }
; #define G8_GOFF(dst, u_) do { _Pragma("unroll") for (int h_ = 0; h_ < 2; ++h_) _Pragma("unroll") for (int i_ = 0; i_ < 2; ++i_) dst[h_][i_] = (unsigned)(S.rowmap[(u_).pm * 256 + h_ * 128 + gR[i_]] * lda + gC[i_]) * 2u; } while (0)
; #define G8_WAIT_V(n) asm volatile("s_waitcnt vmcnt(" #n ")" ::: "memory")
; #define G8_BAR __builtin_amdgcn_s_barrier()
; template <int lda, int ldb, class Epi, class Sched>
; __device__ __forceinline__ void gemm_phase(LAS unsigned char* lds, int wid, int lane, const char* baseA, const char* baseB, const Sched& S, const Epi& E) {
;     ...
;     G8_STAGE(G8_SB(0, 0), cB, voffB); if constexpr (!Epi::HALFN) { G8_STAGE(G8_SB(0, 1), cB + hstepB, voffB); } G8_STAGE_A(G8_SA(0, 0), cA, 0, false); G8_STAGE_A(G8_SA(0, 1), cA, 1, false);
;     if (wr == 1) G8_BAR;
;     G8_WAIT_V(2); G8_BAR;
;     G8_STAGE(G8_SB(1, 0), cB + kstep, voffB); G8_STAGE_A(G8_SA(1, 0), cA + kstep, 0, false); if constexpr (!Epi::HALFN) { G8_STAGE(G8_SB(1, 1), cB + hstepB + kstep, voffB); }
;     if constexpr (Epi::HALFN) { G8_WAIT_V(4); } else { G8_WAIT_V(6); } G8_BAR;
;     for (;;) {
;         const bool has_next = S.next(ui + 1, nxt);
;         const char* nA = Sched::GATHER ? baseA : (has_next ? baseA + nxt.ao : cA); const char* nB = has_next ? baseB + nxt.bo : cB;
;         if constexpr (Sched::GATHER) { if (has_next) { G8_GOFF(gnxt, nxt); } else { _Pragma("unroll") for (int h_ = 0; h_ < 2; ++h_) _Pragma("unroll") for (int i_ = 0; i_ < 2; ++i_) gnxt[h_][i_] = goff[h_][i_]; } }
;         int nt = cur.nt; asm volatile("" : "+s"(nt));
;     __device__ bool next(int i, g8::Unit& u) const { if (i >= cnt) return false; const int id = base + i, pm = id >> 4, pn = id & 15;
;         u.ao = (unsigned)pm * (unsigned)(g8::BM * 512 * 2); u.bo = (unsigned)pn * (unsigned)(g8::BM * 512 * 2); u.nt = 512 / g8::BK; u.pm = pm; u.pn = pn; u.tag = 0; return true; }
.LBB0_1075:
	s_or_b64 exec, exec, s[10:11]
	s_waitcnt lgkmcnt(0)
	s_barrier
	ds_read_b32 v0, v183
	s_movk_i32 s4, 0x3ff
	s_mov_b64 s[10:11], -1
	s_waitcnt lgkmcnt(0)
	s_barrier
	v_cmp_lt_i32_e32 vcc, s4, v0
	v_readfirstlane_b32 s3, v0
	s_cbranch_vccnz .LBB0_1070
	s_ashr_i32 s59, s3, 4
	s_and_b32 s3, s3, 15
	s_lshl_b32 s4, s3, 18
	s_lshl_b32 s10, s59, 18
	s_add_u32 s52, s31, s4
	s_addc_u32 s53, s58, 0
	s_add_i32 s60, s27, 0x10000
	s_add_i32 s61, s27, 0x12000
	v_mov_b32_e32 v18, v31
	v_mov_b32_e32 v213, 0x7f7f7f7f
	v_lshl_add_u64 v[0:1], s[52:53], 0, v[160:161]
	s_mov_b32 m0, s60
	s_add_u32 s16, s52, 0x20000
	s_load_dwordx2 s[14:15], s[42:43], 0x70
	global_load_lds_dwordx4 v[0:1], off
	v_lshl_add_u64 v[2:3], s[52:53], 0, v[156:157]
	s_mov_b32 m0, s61
	s_addc_u32 s17, s53, 0
	s_add_i32 s62, s27, 0x14000
	s_add_i32 s63, s27, 0x16000
	global_load_lds_dwordx4 v[2:3], off
	v_lshl_add_u64 v[4:5], s[16:17], 0, v[160:161]
	s_mov_b32 m0, s62
	s_add_u32 s54, s2, s10
	global_load_lds_dwordx4 v[4:5], off
	v_lshl_add_u64 v[4:5], s[16:17], 0, v[156:157]
	s_mov_b32 m0, s63
	s_addc_u32 s55, s13, 0
	s_add_i32 s64, s27, 0x2000
	global_load_lds_dwordx4 v[4:5], off
	v_lshl_add_u64 v[6:7], s[54:55], 0, v[162:163]
	s_mov_b32 m0, s27
	s_add_u32 s16, s54, 0x20000
	global_load_lds_dwordx4 v[6:7], off
	v_lshl_add_u64 v[4:5], s[54:55], 0, v[158:159]
	s_mov_b32 m0, s64
	s_addc_u32 s17, s55, 0
	s_add_i32 s65, s27, 0x4000
	global_load_lds_dwordx4 v[4:5], off
	v_lshl_add_u64 v[8:9], s[16:17], 0, v[162:163]
	s_mov_b32 m0, s65
	s_add_i32 s66, s27, 0x6000
	global_load_lds_dwordx4 v[8:9], off
	v_lshl_add_u64 v[8:9], s[16:17], 0, v[158:159]
	s_mov_b32 m0, s66
	v_readlane_b32 s16, v254, 2
	global_load_lds_dwordx4 v[8:9], off
	v_readlane_b32 s17, v254, 3
	s_andn2_b64 vcc, exec, s[16:17]
	s_mov_b32 s11, s5
	v_cndmask_b32_e64 v8, 0, 1, s[16:17]
	v_cmp_ne_u32_e64 s[40:41], 1, v8
	s_cbranch_vccnz .LBB0_1078
	s_barrier
.LBB0_1078:
	s_waitcnt lgkmcnt(0)
	s_add_u32 s14, s14, s48
	s_addc_u32 s15, s15, s49
	v_mbcnt_lo_u32_b32 v149, -1, 0
	v_mbcnt_hi_u32_b32 v149, -1, v149
	s_lshl_b32 s16, s3, 8
	s_or_b32 s16, s16, s95
	v_and_b32_e32 v150, 31, v149
	v_lshrrev_b32_e32 v149, 5, v149
	v_lshl_or_b32 v149, v149, 7, v150
	v_add_lshl_u32 v154, v149, s16, 2
	v_mov_b32_e32 v155, 0
	s_lshr_b32 s16, s27, 1
	s_add_i32 s16, s16, 0x23000
	v_lshl_add_u64 v[154:155], s[14:15], 0, v[154:155]
	s_mov_b32 m0, s16
	s_nop 0
	global_load_lds_dword v[154:155], off
	s_add_i32 s67, s27, 0x18000
	v_lshl_add_u64 v[0:1], v[0:1], 0, s[22:23]
	s_mov_b32 m0, s67
	s_add_i32 s68, s27, 0x1a000
	s_waitcnt vmcnt(3)
	s_barrier
	global_load_lds_dwordx4 v[0:1], off
	v_lshl_add_u64 v[0:1], v[2:3], 0, s[22:23]
	s_mov_b32 m0, s68
	s_add_i32 s69, s27, 0x8000
	s_add_i32 s70, s27, 0xa000
	global_load_lds_dwordx4 v[0:1], off
	v_lshl_add_u64 v[0:1], v[6:7], 0, s[22:23]
	s_mov_b32 m0, s69
	s_add_u32 s16, s52, 0x20080
	global_load_lds_dwordx4 v[0:1], off
	v_lshl_add_u64 v[0:1], v[4:5], 0, s[22:23]
	s_mov_b32 m0, s70
	s_addc_u32 s17, s53, 0
	s_add_i32 s71, s27, 0x1c000
	global_load_lds_dwordx4 v[0:1], off
	v_lshl_add_u64 v[0:1], s[16:17], 0, v[160:161]
	s_mov_b32 m0, s71
	s_add_i32 s72, s27, 0x1e000
	global_load_lds_dwordx4 v[0:1], off
	v_lshl_add_u64 v[0:1], s[16:17], 0, v[156:157]
	s_mov_b32 m0, s72
	s_or_b32 s73, s3, 1
	global_load_lds_dwordx4 v[0:1], off
	s_waitcnt vmcnt(7)
	v_mov_b32_e32 v19, v18
	v_mov_b32_e32 v20, v18
	v_mov_b32_e32 v21, v18
	s_lshl_b32 s74, s73, 18
	s_mov_b64 s[16:17], 0
	s_mov_b32 s21, s3
	s_mov_b32 s28, s59
	s_lshl_b32 s29, s3, 18
	s_mov_b32 s4, s10
	s_mov_b32 s20, s59
	v_mov_b32_e32 v16, v18
	s_barrier
	s_branch .LBB0_1081

; __device__ __forceinline__ float fast_sigmoid(float z) { return __builtin_amdgcn_rcpf(1.f + __builtin_amdgcn_exp2f(-z * LOG2E)); }
;     static __device__ __forceinline__ unsigned q8(float z) { return (unsigned)(fast_sigmoid(z) * 255.f + 0.5f); }
;     __device__ __forceinline__ void operator()(const f32x4 (&acc)[2][2][4][2], const g8::Unit& u, int wr, int wc, int fr, int fq) const {
;         const int row0 = u.pm * 256 + wr * 64 + fr, col0 = u.pn * 256 + wc * 32 + 8 * fq;
; #pragma unroll
;         for (int bj = 0; bj < 2; ++bj) {
;             const f32x4 bv0 = *(const f32x4*)(bgate + col0 + bj * 128), bv1 = *(const f32x4*)(bgate + col0 + bj * 128 + 4);
; #pragma unroll
;             for (int ai = 0; ai < 2; ++ai)
; #pragma unroll
;                 for (int m = 0; m < 4; ++m) { const int row = row0 + ai * 128 + m * 16; unsigned char* rp = GT + (size_t)row * 4096 + col0 + bj * 128;
;                     const f32x4 v0 = acc[ai][bj][m][0] * 0.03125f + bv0, v1 = acc[ai][bj][m][1] * 0.03125f + bv1;
;                     u32x2 w; w.x = q8(v0[0]) | (q8(v0[1]) << 8) | (q8(v0[2]) << 16) | (q8(v0[3]) << 24); w.y = q8(v1[0]) | (q8(v1[1]) << 8) | (q8(v1[2]) << 16) | (q8(v1[3]) << 24);
;                     *(u32x2*)rp = w; } }
; __device__ __forceinline__ void gate_batches(LAS unsigned char* lds, int wv, int l, int max_batches) {
;     ...
;         if (F.tid == 0) *gslot = (int)__hip_atomic_fetch_add(qg, 1u, __ATOMIC_RELAXED, __HIP_MEMORY_SCOPE_AGENT);
.LBB0_1088:
	s_and_b64 vcc, exec, s[16:17]
	s_cbranch_vccnz .Lgq_skip
	s_and_saveexec_b64 s[52:53], s[38:39]
	v_mov_b32_e32 v150, 1
	global_atomic_add v150, v31, v150, s[44:45] sc0
	s_or_b64 exec, exec, s[52:53]
.Lgq_skip:
	s_mov_b32 s4, -1
	s_mov_b32 s52, 0
	s_lshr_b32 s53, s27, 1
	s_lshl_b32 s52, s52, 8
	s_add_i32 s53, s53, 0x23000
	s_add_i32 s52, s52, s53
	s_lshl_b32 s3, s3, 8
	v_mbcnt_lo_u32_b32 v0, s4, 0
	v_mbcnt_hi_u32_b32 v0, s4, v0
	s_lshl_b32 s4, s20, 8
	s_add_i32 s4, s4, s9
	v_lshrrev_b32_e32 v168, 2, v0
	v_and_b32_e32 v170, 3, v0
	v_and_b32_e32 v17, 60, v0
	v_or_b32_e32 v168, s4, v168
	v_lshrrev_b32_e32 v0, 1, v0
	s_or_b32 s3, s3, s95
	v_lshl_or_b32 v17, v170, 6, v17
	v_and_b32_e32 v0, 56, v0
	v_lshl_add_u32 v170, v170, 3, s3
	v_lshl_add_u32 v12, v0, 2, s52
	ds_read_b128 v[4:7], v12
	ds_read_b128 v[0:3], v12 offset:16
	ds_read_b128 v[184:187], v12 offset:128
	ds_read_b128 v[188:191], v12 offset:144
	v_ashrrev_i32_e32 v171, 31, v170
	v_ashrrev_i32_e32 v169, 31, v168
	v_lshlrev_b64 v[8:9], 12, v[168:169]
	s_mov_b64 s[52:53], 0x10000
	s_mov_b64 vcc, 0x80000
	v_lshl_add_u64 v[8:9], s[46:47], 0, v[8:9]
	s_mov_b32 s20, 0xbd38aa3b
	s_mov_b32 s21, 0x3b808081
	v_lshl_add_u64 v[8:9], v[8:9], 0, v[170:171]
	v_lshl_add_u64 v[10:11], v[8:9], 0, s[52:53]
	v_lshl_add_u64 v[192:193], v[8:9], 0, vcc
	v_lshl_add_u64 v[14:15], v[10:11], 0, s[52:53]
	v_lshl_add_u64 v[194:195], v[192:193], 0, s[52:53]
	v_lshl_add_u64 v[168:169], v[14:15], 0, s[52:53]
	v_lshl_add_u64 v[196:197], v[194:195], 0, s[52:53]
	v_lshl_add_u64 v[198:199], v[196:197], 0, s[52:53]
	s_waitcnt lgkmcnt(0)
	v_mul_f32_e32 v0, 0xbfb8aa3b, v0
	v_mul_f32_e32 v1, 0xbfb8aa3b, v1
	v_mul_f32_e32 v2, 0xbfb8aa3b, v2
	v_mul_f32_e32 v3, 0xbfb8aa3b, v3
	v_mul_f32_e32 v4, 0xbfb8aa3b, v4
	v_mul_f32_e32 v5, 0xbfb8aa3b, v5
	v_mul_f32_e32 v6, 0xbfb8aa3b, v6
	v_mul_f32_e32 v7, 0xbfb8aa3b, v7
	v_mul_f32_e32 v184, 0xbfb8aa3b, v184
	v_mul_f32_e32 v185, 0xbfb8aa3b, v185
	v_mul_f32_e32 v186, 0xbfb8aa3b, v186
	v_mul_f32_e32 v187, 0xbfb8aa3b, v187
	v_mul_f32_e32 v188, 0xbfb8aa3b, v188
	v_mul_f32_e32 v189, 0xbfb8aa3b, v189
	v_mul_f32_e32 v190, 0xbfb8aa3b, v190
	v_mul_f32_e32 v191, 0xbfb8aa3b, v191
	v_pk_fma_f32 v[144:145], v[144:145], s[20:21], v[4:5] op_sel_hi:[1,0,1]
	v_pk_fma_f32 v[146:147], v[146:147], s[20:21], v[6:7] op_sel_hi:[1,0,1]
	v_pk_fma_f32 v[140:141], v[140:141], s[20:21], v[0:1] op_sel_hi:[1,0,1]
	v_pk_fma_f32 v[142:143], v[142:143], s[20:21], v[2:3] op_sel_hi:[1,0,1]
	v_pk_fma_f32 v[136:137], v[136:137], s[20:21], v[4:5] op_sel_hi:[1,0,1]
	v_pk_fma_f32 v[138:139], v[138:139], s[20:21], v[6:7] op_sel_hi:[1,0,1]
	v_pk_fma_f32 v[132:133], v[132:133], s[20:21], v[0:1] op_sel_hi:[1,0,1]
	v_pk_fma_f32 v[134:135], v[134:135], s[20:21], v[2:3] op_sel_hi:[1,0,1]
	v_exp_f32_e32 v144, v144
	v_exp_f32_e32 v145, v145
	v_exp_f32_e32 v146, v146
	v_exp_f32_e32 v147, v147
	v_exp_f32_e32 v140, v140
	v_exp_f32_e32 v141, v141
	v_exp_f32_e32 v142, v142
	v_exp_f32_e32 v143, v143
	v_exp_f32_e32 v136, v136
	v_exp_f32_e32 v137, v137
	v_exp_f32_e32 v138, v138
	v_exp_f32_e32 v139, v139
	v_exp_f32_e32 v132, v132
	v_exp_f32_e32 v133, v133
	v_exp_f32_e32 v134, v134
	v_exp_f32_e32 v135, v135
	v_fma_f32 v144, v144, s21, s21
	v_fma_f32 v145, v145, s21, s21
	v_fma_f32 v146, v146, s21, s21
	v_fma_f32 v147, v147, s21, s21
	v_fma_f32 v140, v140, s21, s21
	v_fma_f32 v141, v141, s21, s21
	v_fma_f32 v142, v142, s21, s21
	v_fma_f32 v143, v143, s21, s21
	v_fma_f32 v136, v136, s21, s21
	v_fma_f32 v137, v137, s21, s21
	v_fma_f32 v138, v138, s21, s21
	v_fma_f32 v139, v139, s21, s21
	v_fma_f32 v132, v132, s21, s21
	v_fma_f32 v133, v133, s21, s21
	v_fma_f32 v134, v134, s21, s21
	v_fma_f32 v135, v135, s21, s21
	v_rcp_f32_e32 v144, v144
	v_rcp_f32_e32 v145, v145
	v_rcp_f32_e32 v146, v146
	v_rcp_f32_e32 v147, v147
	v_rcp_f32_e32 v140, v140
	v_rcp_f32_e32 v141, v141
	v_rcp_f32_e32 v142, v142
	v_rcp_f32_e32 v143, v143
	v_rcp_f32_e32 v136, v136
	v_rcp_f32_e32 v137, v137
	v_rcp_f32_e32 v138, v138
	v_rcp_f32_e32 v139, v139
	v_rcp_f32_e32 v132, v132
	v_rcp_f32_e32 v133, v133
	v_rcp_f32_e32 v134, v134
	v_rcp_f32_e32 v135, v135
	v_cvt_rpi_i32_f32_e32 v144, v144
	v_cvt_rpi_i32_f32_e32 v136, v136
	v_cvt_rpi_i32_f32_sdwa v144, v145 dst_sel:BYTE_1 dst_unused:UNUSED_PRESERVE src0_sel:DWORD
	v_cvt_rpi_i32_f32_sdwa v136, v137 dst_sel:BYTE_1 dst_unused:UNUSED_PRESERVE src0_sel:DWORD
	v_cvt_rpi_i32_f32_e32 v145, v140
	v_cvt_rpi_i32_f32_e32 v137, v132
	v_cvt_rpi_i32_f32_sdwa v144, v146 dst_sel:BYTE_2 dst_unused:UNUSED_PRESERVE src0_sel:DWORD
	v_cvt_rpi_i32_f32_sdwa v136, v138 dst_sel:BYTE_2 dst_unused:UNUSED_PRESERVE src0_sel:DWORD
	v_cvt_rpi_i32_f32_sdwa v145, v141 dst_sel:BYTE_1 dst_unused:UNUSED_PRESERVE src0_sel:DWORD
	v_cvt_rpi_i32_f32_sdwa v137, v133 dst_sel:BYTE_1 dst_unused:UNUSED_PRESERVE src0_sel:DWORD
	v_cvt_rpi_i32_f32_sdwa v144, v147 dst_sel:BYTE_3 dst_unused:UNUSED_PRESERVE src0_sel:DWORD
	v_cvt_rpi_i32_f32_sdwa v136, v139 dst_sel:BYTE_3 dst_unused:UNUSED_PRESERVE src0_sel:DWORD
	v_cvt_rpi_i32_f32_sdwa v145, v142 dst_sel:BYTE_2 dst_unused:UNUSED_PRESERVE src0_sel:DWORD
	v_cvt_rpi_i32_f32_sdwa v137, v134 dst_sel:BYTE_2 dst_unused:UNUSED_PRESERVE src0_sel:DWORD
	v_cvt_rpi_i32_f32_sdwa v145, v143 dst_sel:BYTE_3 dst_unused:UNUSED_PRESERVE src0_sel:DWORD
	v_cvt_rpi_i32_f32_sdwa v137, v135 dst_sel:BYTE_3 dst_unused:UNUSED_PRESERVE src0_sel:DWORD
	ds_bpermute_b32 v144, v17, v144
	ds_bpermute_b32 v145, v17, v145
	ds_bpermute_b32 v136, v17, v136
	ds_bpermute_b32 v137, v17, v137
	v_pk_fma_f32 v[128:129], v[128:129], s[20:21], v[4:5] op_sel_hi:[1,0,1]
	v_pk_fma_f32 v[130:131], v[130:131], s[20:21], v[6:7] op_sel_hi:[1,0,1]
; __device__ __forceinline__ float fast_sigmoid(float z) { return __builtin_amdgcn_rcpf(1.f + __builtin_amdgcn_exp2f(-z * LOG2E)); }
;     static __device__ __forceinline__ unsigned q8(float z) { return (unsigned)(fast_sigmoid(z) * 255.f + 0.5f); }
;     __device__ __forceinline__ void operator()(const f32x4 (&acc)[2][2][4][2], const g8::Unit& u, int wr, int wc, int fr, int fq) const {
;         const int row0 = u.pm * 256 + wr * 64 + fr, col0 = u.pn * 256 + wc * 32 + 8 * fq;
; #pragma unroll
;         for (int bj = 0; bj < 2; ++bj) {
;             const f32x4 bv0 = *(const f32x4*)(bgate + col0 + bj * 128), bv1 = *(const f32x4*)(bgate + col0 + bj * 128 + 4);
; #pragma unroll
;             for (int ai = 0; ai < 2; ++ai)
; #pragma unroll
;                 for (int m = 0; m < 4; ++m) { const int row = row0 + ai * 128 + m * 16; unsigned char* rp = GT + (size_t)row * 4096 + col0 + bj * 128;
;                     const f32x4 v0 = acc[ai][bj][m][0] * 0.03125f + bv0, v1 = acc[ai][bj][m][1] * 0.03125f + bv1;
;                     u32x2 w; w.x = q8(v0[0]) | (q8(v0[1]) << 8) | (q8(v0[2]) << 16) | (q8(v0[3]) << 24); w.y = q8(v1[0]) | (q8(v1[1]) << 8) | (q8(v1[2]) << 16) | (q8(v1[3]) << 24);
;                     *(u32x2*)rp = w; } }
	v_pk_fma_f32 v[124:125], v[124:125], s[20:21], v[0:1] op_sel_hi:[1,0,1]
	v_pk_fma_f32 v[126:127], v[126:127], s[20:21], v[2:3] op_sel_hi:[1,0,1]
	v_pk_fma_f32 v[120:121], v[120:121], s[20:21], v[4:5] op_sel_hi:[1,0,1]
	v_pk_fma_f32 v[122:123], v[122:123], s[20:21], v[6:7] op_sel_hi:[1,0,1]
	v_pk_fma_f32 v[116:117], v[116:117], s[20:21], v[0:1] op_sel_hi:[1,0,1]
	v_pk_fma_f32 v[118:119], v[118:119], s[20:21], v[2:3] op_sel_hi:[1,0,1]
	v_exp_f32_e32 v128, v128
	v_exp_f32_e32 v129, v129
	v_exp_f32_e32 v130, v130
	v_exp_f32_e32 v131, v131
	v_exp_f32_e32 v124, v124
	v_exp_f32_e32 v125, v125
	v_exp_f32_e32 v126, v126
	v_exp_f32_e32 v127, v127
	v_exp_f32_e32 v120, v120
	v_exp_f32_e32 v121, v121
	v_exp_f32_e32 v122, v122
	v_exp_f32_e32 v123, v123
	v_exp_f32_e32 v116, v116
	v_exp_f32_e32 v117, v117
	v_exp_f32_e32 v118, v118
	v_exp_f32_e32 v119, v119
	v_fma_f32 v128, v128, s21, s21
	v_fma_f32 v129, v129, s21, s21
	v_fma_f32 v130, v130, s21, s21
	v_fma_f32 v131, v131, s21, s21
	v_fma_f32 v124, v124, s21, s21
	v_fma_f32 v125, v125, s21, s21
	v_fma_f32 v126, v126, s21, s21
	v_fma_f32 v127, v127, s21, s21
	v_fma_f32 v120, v120, s21, s21
	v_fma_f32 v121, v121, s21, s21
	v_fma_f32 v122, v122, s21, s21
	v_fma_f32 v123, v123, s21, s21
	v_fma_f32 v116, v116, s21, s21
	v_fma_f32 v117, v117, s21, s21
	v_fma_f32 v118, v118, s21, s21
	v_fma_f32 v119, v119, s21, s21
	v_rcp_f32_e32 v128, v128
	v_rcp_f32_e32 v129, v129
	v_rcp_f32_e32 v130, v130
	v_rcp_f32_e32 v131, v131
	v_rcp_f32_e32 v124, v124
	v_rcp_f32_e32 v125, v125
	v_rcp_f32_e32 v126, v126
	v_rcp_f32_e32 v127, v127
	v_rcp_f32_e32 v120, v120
	v_rcp_f32_e32 v121, v121
	v_rcp_f32_e32 v122, v122
	v_rcp_f32_e32 v123, v123
	v_rcp_f32_e32 v116, v116
	v_rcp_f32_e32 v117, v117
	v_rcp_f32_e32 v118, v118
	v_rcp_f32_e32 v119, v119
	v_cvt_rpi_i32_f32_e32 v128, v128
	v_cvt_rpi_i32_f32_e32 v120, v120
	v_cvt_rpi_i32_f32_sdwa v128, v129 dst_sel:BYTE_1 dst_unused:UNUSED_PRESERVE src0_sel:DWORD
	v_cvt_rpi_i32_f32_sdwa v120, v121 dst_sel:BYTE_1 dst_unused:UNUSED_PRESERVE src0_sel:DWORD
	v_cvt_rpi_i32_f32_e32 v129, v124
	v_cvt_rpi_i32_f32_e32 v121, v116
	v_cvt_rpi_i32_f32_sdwa v128, v130 dst_sel:BYTE_2 dst_unused:UNUSED_PRESERVE src0_sel:DWORD
	v_cvt_rpi_i32_f32_sdwa v120, v122 dst_sel:BYTE_2 dst_unused:UNUSED_PRESERVE src0_sel:DWORD
	v_cvt_rpi_i32_f32_sdwa v129, v125 dst_sel:BYTE_1 dst_unused:UNUSED_PRESERVE src0_sel:DWORD
	v_cvt_rpi_i32_f32_sdwa v121, v117 dst_sel:BYTE_1 dst_unused:UNUSED_PRESERVE src0_sel:DWORD
	v_cvt_rpi_i32_f32_sdwa v128, v131 dst_sel:BYTE_3 dst_unused:UNUSED_PRESERVE src0_sel:DWORD
	v_cvt_rpi_i32_f32_sdwa v120, v123 dst_sel:BYTE_3 dst_unused:UNUSED_PRESERVE src0_sel:DWORD
	v_cvt_rpi_i32_f32_sdwa v129, v126 dst_sel:BYTE_2 dst_unused:UNUSED_PRESERVE src0_sel:DWORD
	v_cvt_rpi_i32_f32_sdwa v121, v118 dst_sel:BYTE_2 dst_unused:UNUSED_PRESERVE src0_sel:DWORD
	v_cvt_rpi_i32_f32_sdwa v129, v127 dst_sel:BYTE_3 dst_unused:UNUSED_PRESERVE src0_sel:DWORD
	v_cvt_rpi_i32_f32_sdwa v121, v119 dst_sel:BYTE_3 dst_unused:UNUSED_PRESERVE src0_sel:DWORD
	ds_bpermute_b32 v128, v17, v128
	ds_bpermute_b32 v129, v17, v129
	ds_bpermute_b32 v120, v17, v120
	ds_bpermute_b32 v121, v17, v121
	s_waitcnt lgkmcnt(4)
	global_store_dwordx2 v[8:9], v[144:145], off
	global_store_dwordx2 v[10:11], v[136:137], off
	v_pk_fma_f32 v[112:113], v[112:113], s[20:21], v[4:5] op_sel_hi:[1,0,1]
	v_pk_fma_f32 v[114:115], v[114:115], s[20:21], v[6:7] op_sel_hi:[1,0,1]
	v_pk_fma_f32 v[108:109], v[108:109], s[20:21], v[0:1] op_sel_hi:[1,0,1]
	v_pk_fma_f32 v[110:111], v[110:111], s[20:21], v[2:3] op_sel_hi:[1,0,1]
	v_pk_fma_f32 v[104:105], v[104:105], s[20:21], v[4:5] op_sel_hi:[1,0,1]
	v_pk_fma_f32 v[106:107], v[106:107], s[20:21], v[6:7] op_sel_hi:[1,0,1]
	v_pk_fma_f32 v[100:101], v[100:101], s[20:21], v[0:1] op_sel_hi:[1,0,1]
	v_pk_fma_f32 v[102:103], v[102:103], s[20:21], v[2:3] op_sel_hi:[1,0,1]
	v_exp_f32_e32 v112, v112
	v_exp_f32_e32 v113, v113
	v_exp_f32_e32 v114, v114
	v_exp_f32_e32 v115, v115
	v_exp_f32_e32 v108, v108
	v_exp_f32_e32 v109, v109
	v_exp_f32_e32 v110, v110
	v_exp_f32_e32 v111, v111
	v_exp_f32_e32 v104, v104
	v_exp_f32_e32 v105, v105
	v_exp_f32_e32 v106, v106
	v_exp_f32_e32 v107, v107
	v_exp_f32_e32 v100, v100
	v_exp_f32_e32 v101, v101
	v_exp_f32_e32 v102, v102
	v_exp_f32_e32 v103, v103
	v_fma_f32 v112, v112, s21, s21
	v_fma_f32 v113, v113, s21, s21
	v_fma_f32 v114, v114, s21, s21
	v_fma_f32 v115, v115, s21, s21
	v_fma_f32 v108, v108, s21, s21
	v_fma_f32 v109, v109, s21, s21
	v_fma_f32 v110, v110, s21, s21
	v_fma_f32 v111, v111, s21, s21
	v_fma_f32 v104, v104, s21, s21
	v_fma_f32 v105, v105, s21, s21
	v_fma_f32 v106, v106, s21, s21
	v_fma_f32 v107, v107, s21, s21
	v_fma_f32 v100, v100, s21, s21
	v_fma_f32 v101, v101, s21, s21
	v_fma_f32 v102, v102, s21, s21
	v_fma_f32 v103, v103, s21, s21
	v_rcp_f32_e32 v112, v112
	v_rcp_f32_e32 v113, v113
	v_rcp_f32_e32 v114, v114
	v_rcp_f32_e32 v115, v115
	v_rcp_f32_e32 v108, v108
	v_rcp_f32_e32 v109, v109
	v_rcp_f32_e32 v110, v110
	v_rcp_f32_e32 v111, v111
	v_rcp_f32_e32 v104, v104
	v_rcp_f32_e32 v105, v105
	v_rcp_f32_e32 v106, v106
	v_rcp_f32_e32 v107, v107
	v_rcp_f32_e32 v100, v100
	v_rcp_f32_e32 v101, v101
	v_rcp_f32_e32 v102, v102
	v_rcp_f32_e32 v103, v103
	v_cvt_rpi_i32_f32_e32 v112, v112
	v_cvt_rpi_i32_f32_e32 v104, v104
	v_cvt_rpi_i32_f32_sdwa v112, v113 dst_sel:BYTE_1 dst_unused:UNUSED_PRESERVE src0_sel:DWORD
	v_cvt_rpi_i32_f32_sdwa v104, v105 dst_sel:BYTE_1 dst_unused:UNUSED_PRESERVE src0_sel:DWORD
	v_cvt_rpi_i32_f32_e32 v113, v108
	v_cvt_rpi_i32_f32_e32 v105, v100
	v_cvt_rpi_i32_f32_sdwa v112, v114 dst_sel:BYTE_2 dst_unused:UNUSED_PRESERVE src0_sel:DWORD
	v_cvt_rpi_i32_f32_sdwa v104, v106 dst_sel:BYTE_2 dst_unused:UNUSED_PRESERVE src0_sel:DWORD
	v_cvt_rpi_i32_f32_sdwa v113, v109 dst_sel:BYTE_1 dst_unused:UNUSED_PRESERVE src0_sel:DWORD
	v_cvt_rpi_i32_f32_sdwa v105, v101 dst_sel:BYTE_1 dst_unused:UNUSED_PRESERVE src0_sel:DWORD
	v_cvt_rpi_i32_f32_sdwa v112, v115 dst_sel:BYTE_3 dst_unused:UNUSED_PRESERVE src0_sel:DWORD
	v_cvt_rpi_i32_f32_sdwa v104, v107 dst_sel:BYTE_3 dst_unused:UNUSED_PRESERVE src0_sel:DWORD
	v_cvt_rpi_i32_f32_sdwa v113, v110 dst_sel:BYTE_2 dst_unused:UNUSED_PRESERVE src0_sel:DWORD
	v_cvt_rpi_i32_f32_sdwa v105, v102 dst_sel:BYTE_2 dst_unused:UNUSED_PRESERVE src0_sel:DWORD
	v_cvt_rpi_i32_f32_sdwa v113, v111 dst_sel:BYTE_3 dst_unused:UNUSED_PRESERVE src0_sel:DWORD
	v_cvt_rpi_i32_f32_sdwa v105, v103 dst_sel:BYTE_3 dst_unused:UNUSED_PRESERVE src0_sel:DWORD
	ds_bpermute_b32 v112, v17, v112
	ds_bpermute_b32 v113, v17, v113
	ds_bpermute_b32 v104, v17, v104
	ds_bpermute_b32 v105, v17, v105
	s_waitcnt lgkmcnt(4)
; __device__ __forceinline__ float fast_sigmoid(float z) { return __builtin_amdgcn_rcpf(1.f + __builtin_amdgcn_exp2f(-z * LOG2E)); }
;     static __device__ __forceinline__ unsigned q8(float z) { return (unsigned)(fast_sigmoid(z) * 255.f + 0.5f); }
;     __device__ __forceinline__ void operator()(const f32x4 (&acc)[2][2][4][2], const g8::Unit& u, int wr, int wc, int fr, int fq) const {
;         const int row0 = u.pm * 256 + wr * 64 + fr, col0 = u.pn * 256 + wc * 32 + 8 * fq;
; #pragma unroll
;         for (int bj = 0; bj < 2; ++bj) {
;             const f32x4 bv0 = *(const f32x4*)(bgate + col0 + bj * 128), bv1 = *(const f32x4*)(bgate + col0 + bj * 128 + 4);
; #pragma unroll
;             for (int ai = 0; ai < 2; ++ai)
; #pragma unroll
;                 for (int m = 0; m < 4; ++m) { const int row = row0 + ai * 128 + m * 16; unsigned char* rp = GT + (size_t)row * 4096 + col0 + bj * 128;
;                     const f32x4 v0 = acc[ai][bj][m][0] * 0.03125f + bv0, v1 = acc[ai][bj][m][1] * 0.03125f + bv1;
;                     u32x2 w; w.x = q8(v0[0]) | (q8(v0[1]) << 8) | (q8(v0[2]) << 16) | (q8(v0[3]) << 24); w.y = q8(v1[0]) | (q8(v1[1]) << 8) | (q8(v1[2]) << 16) | (q8(v1[3]) << 24);
;                     *(u32x2*)rp = w; } }
	global_store_dwordx2 v[14:15], v[128:129], off
	global_store_dwordx2 v[168:169], v[120:121], off
	v_pk_fma_f32 v[96:97], v[96:97], s[20:21], v[4:5] op_sel_hi:[1,0,1]
	v_pk_fma_f32 v[98:99], v[98:99], s[20:21], v[6:7] op_sel_hi:[1,0,1]
	v_pk_fma_f32 v[92:93], v[92:93], s[20:21], v[0:1] op_sel_hi:[1,0,1]
	v_pk_fma_f32 v[94:95], v[94:95], s[20:21], v[2:3] op_sel_hi:[1,0,1]
	v_pk_fma_f32 v[88:89], v[88:89], s[20:21], v[4:5] op_sel_hi:[1,0,1]
	v_pk_fma_f32 v[90:91], v[90:91], s[20:21], v[6:7] op_sel_hi:[1,0,1]
	v_pk_fma_f32 v[84:85], v[84:85], s[20:21], v[0:1] op_sel_hi:[1,0,1]
	v_pk_fma_f32 v[86:87], v[86:87], s[20:21], v[2:3] op_sel_hi:[1,0,1]
	v_exp_f32_e32 v96, v96
	v_exp_f32_e32 v97, v97
	v_exp_f32_e32 v98, v98
	v_exp_f32_e32 v99, v99
	v_exp_f32_e32 v92, v92
	v_exp_f32_e32 v93, v93
	v_exp_f32_e32 v94, v94
	v_exp_f32_e32 v95, v95
	v_exp_f32_e32 v88, v88
	v_exp_f32_e32 v89, v89
	v_exp_f32_e32 v90, v90
	v_exp_f32_e32 v91, v91
	v_exp_f32_e32 v84, v84
	v_exp_f32_e32 v85, v85
	v_exp_f32_e32 v86, v86
	v_exp_f32_e32 v87, v87
	v_fma_f32 v96, v96, s21, s21
	v_fma_f32 v97, v97, s21, s21
	v_fma_f32 v98, v98, s21, s21
	v_fma_f32 v99, v99, s21, s21
	v_fma_f32 v92, v92, s21, s21
	v_fma_f32 v93, v93, s21, s21
	v_fma_f32 v94, v94, s21, s21
	v_fma_f32 v95, v95, s21, s21
	v_fma_f32 v88, v88, s21, s21
	v_fma_f32 v89, v89, s21, s21
	v_fma_f32 v90, v90, s21, s21
	v_fma_f32 v91, v91, s21, s21
	v_fma_f32 v84, v84, s21, s21
	v_fma_f32 v85, v85, s21, s21
	v_fma_f32 v86, v86, s21, s21
	v_fma_f32 v87, v87, s21, s21
	v_rcp_f32_e32 v96, v96
	v_rcp_f32_e32 v97, v97
	v_rcp_f32_e32 v98, v98
	v_rcp_f32_e32 v99, v99
	v_rcp_f32_e32 v92, v92
	v_rcp_f32_e32 v93, v93
	v_rcp_f32_e32 v94, v94
	v_rcp_f32_e32 v95, v95
	v_rcp_f32_e32 v88, v88
	v_rcp_f32_e32 v89, v89
	v_rcp_f32_e32 v90, v90
	v_rcp_f32_e32 v91, v91
	v_rcp_f32_e32 v84, v84
	v_rcp_f32_e32 v85, v85
	v_rcp_f32_e32 v86, v86
	v_rcp_f32_e32 v87, v87
	v_cvt_rpi_i32_f32_e32 v96, v96
	v_cvt_rpi_i32_f32_e32 v88, v88
	v_cvt_rpi_i32_f32_sdwa v96, v97 dst_sel:BYTE_1 dst_unused:UNUSED_PRESERVE src0_sel:DWORD
	v_cvt_rpi_i32_f32_sdwa v88, v89 dst_sel:BYTE_1 dst_unused:UNUSED_PRESERVE src0_sel:DWORD
	v_cvt_rpi_i32_f32_e32 v97, v92
	v_cvt_rpi_i32_f32_e32 v89, v84
	v_cvt_rpi_i32_f32_sdwa v96, v98 dst_sel:BYTE_2 dst_unused:UNUSED_PRESERVE src0_sel:DWORD
	v_cvt_rpi_i32_f32_sdwa v88, v90 dst_sel:BYTE_2 dst_unused:UNUSED_PRESERVE src0_sel:DWORD
	v_cvt_rpi_i32_f32_sdwa v97, v93 dst_sel:BYTE_1 dst_unused:UNUSED_PRESERVE src0_sel:DWORD
	v_cvt_rpi_i32_f32_sdwa v89, v85 dst_sel:BYTE_1 dst_unused:UNUSED_PRESERVE src0_sel:DWORD
	v_cvt_rpi_i32_f32_sdwa v96, v99 dst_sel:BYTE_3 dst_unused:UNUSED_PRESERVE src0_sel:DWORD
	v_cvt_rpi_i32_f32_sdwa v88, v91 dst_sel:BYTE_3 dst_unused:UNUSED_PRESERVE src0_sel:DWORD
	v_cvt_rpi_i32_f32_sdwa v97, v94 dst_sel:BYTE_2 dst_unused:UNUSED_PRESERVE src0_sel:DWORD
	v_cvt_rpi_i32_f32_sdwa v89, v86 dst_sel:BYTE_2 dst_unused:UNUSED_PRESERVE src0_sel:DWORD
	v_cvt_rpi_i32_f32_sdwa v97, v95 dst_sel:BYTE_3 dst_unused:UNUSED_PRESERVE src0_sel:DWORD
	v_cvt_rpi_i32_f32_sdwa v89, v87 dst_sel:BYTE_3 dst_unused:UNUSED_PRESERVE src0_sel:DWORD
	ds_bpermute_b32 v96, v17, v96
	ds_bpermute_b32 v97, v17, v97
	ds_bpermute_b32 v88, v17, v88
	ds_bpermute_b32 v89, v17, v89
	s_waitcnt lgkmcnt(4)
	global_store_dwordx2 v[192:193], v[112:113], off
	global_store_dwordx2 v[194:195], v[104:105], off
	v_pk_fma_f32 v[80:81], v[80:81], s[20:21], v[184:185] op_sel_hi:[1,0,1]
	v_pk_fma_f32 v[82:83], v[82:83], s[20:21], v[186:187] op_sel_hi:[1,0,1]
	v_pk_fma_f32 v[76:77], v[76:77], s[20:21], v[188:189] op_sel_hi:[1,0,1]
	v_pk_fma_f32 v[78:79], v[78:79], s[20:21], v[190:191] op_sel_hi:[1,0,1]
	v_pk_fma_f32 v[72:73], v[72:73], s[20:21], v[184:185] op_sel_hi:[1,0,1]
	v_pk_fma_f32 v[74:75], v[74:75], s[20:21], v[186:187] op_sel_hi:[1,0,1]
	v_pk_fma_f32 v[68:69], v[68:69], s[20:21], v[188:189] op_sel_hi:[1,0,1]
	v_pk_fma_f32 v[70:71], v[70:71], s[20:21], v[190:191] op_sel_hi:[1,0,1]
	v_exp_f32_e32 v80, v80
	v_exp_f32_e32 v81, v81
	v_exp_f32_e32 v82, v82
	v_exp_f32_e32 v83, v83
	v_exp_f32_e32 v76, v76
	v_exp_f32_e32 v77, v77
	v_exp_f32_e32 v78, v78
	v_exp_f32_e32 v79, v79
	v_exp_f32_e32 v72, v72
	v_exp_f32_e32 v73, v73
	v_exp_f32_e32 v74, v74
	v_exp_f32_e32 v75, v75
	v_exp_f32_e32 v68, v68
	v_exp_f32_e32 v69, v69
	v_exp_f32_e32 v70, v70
	v_exp_f32_e32 v71, v71
	v_fma_f32 v80, v80, s21, s21
	v_fma_f32 v81, v81, s21, s21
	v_fma_f32 v82, v82, s21, s21
	v_fma_f32 v83, v83, s21, s21
	v_fma_f32 v76, v76, s21, s21
	v_fma_f32 v77, v77, s21, s21
	v_fma_f32 v78, v78, s21, s21
	v_fma_f32 v79, v79, s21, s21
	v_fma_f32 v72, v72, s21, s21
	v_fma_f32 v73, v73, s21, s21
	v_fma_f32 v74, v74, s21, s21
	v_fma_f32 v75, v75, s21, s21
	v_fma_f32 v68, v68, s21, s21
	v_fma_f32 v69, v69, s21, s21
	v_fma_f32 v70, v70, s21, s21
	v_fma_f32 v71, v71, s21, s21
	v_rcp_f32_e32 v80, v80
	v_rcp_f32_e32 v81, v81
	v_rcp_f32_e32 v82, v82
	v_rcp_f32_e32 v83, v83
	v_rcp_f32_e32 v76, v76
	v_rcp_f32_e32 v77, v77
	v_rcp_f32_e32 v78, v78
	v_rcp_f32_e32 v79, v79
	v_rcp_f32_e32 v72, v72
	v_rcp_f32_e32 v73, v73
	v_rcp_f32_e32 v74, v74
	v_rcp_f32_e32 v75, v75
	v_rcp_f32_e32 v68, v68
	v_rcp_f32_e32 v69, v69
	v_rcp_f32_e32 v70, v70
	v_rcp_f32_e32 v71, v71
	v_cvt_rpi_i32_f32_e32 v80, v80
	v_cvt_rpi_i32_f32_e32 v72, v72
	v_cvt_rpi_i32_f32_sdwa v80, v81 dst_sel:BYTE_1 dst_unused:UNUSED_PRESERVE src0_sel:DWORD
	v_cvt_rpi_i32_f32_sdwa v72, v73 dst_sel:BYTE_1 dst_unused:UNUSED_PRESERVE src0_sel:DWORD
	v_cvt_rpi_i32_f32_e32 v81, v76
	v_cvt_rpi_i32_f32_e32 v73, v68
	v_cvt_rpi_i32_f32_sdwa v80, v82 dst_sel:BYTE_2 dst_unused:UNUSED_PRESERVE src0_sel:DWORD
	v_cvt_rpi_i32_f32_sdwa v72, v74 dst_sel:BYTE_2 dst_unused:UNUSED_PRESERVE src0_sel:DWORD
	v_cvt_rpi_i32_f32_sdwa v81, v77 dst_sel:BYTE_1 dst_unused:UNUSED_PRESERVE src0_sel:DWORD
	v_cvt_rpi_i32_f32_sdwa v73, v69 dst_sel:BYTE_1 dst_unused:UNUSED_PRESERVE src0_sel:DWORD
	v_cvt_rpi_i32_f32_sdwa v80, v83 dst_sel:BYTE_3 dst_unused:UNUSED_PRESERVE src0_sel:DWORD
	v_cvt_rpi_i32_f32_sdwa v72, v75 dst_sel:BYTE_3 dst_unused:UNUSED_PRESERVE src0_sel:DWORD
	v_cvt_rpi_i32_f32_sdwa v81, v78 dst_sel:BYTE_2 dst_unused:UNUSED_PRESERVE src0_sel:DWORD
	v_cvt_rpi_i32_f32_sdwa v73, v70 dst_sel:BYTE_2 dst_unused:UNUSED_PRESERVE src0_sel:DWORD
	v_cvt_rpi_i32_f32_sdwa v81, v79 dst_sel:BYTE_3 dst_unused:UNUSED_PRESERVE src0_sel:DWORD
	v_cvt_rpi_i32_f32_sdwa v73, v71 dst_sel:BYTE_3 dst_unused:UNUSED_PRESERVE src0_sel:DWORD
	ds_bpermute_b32 v80, v17, v80
	ds_bpermute_b32 v81, v17, v81
	ds_bpermute_b32 v72, v17, v72
	ds_bpermute_b32 v73, v17, v73
	s_waitcnt lgkmcnt(4)
; __device__ __forceinline__ float fast_sigmoid(float z) { return __builtin_amdgcn_rcpf(1.f + __builtin_amdgcn_exp2f(-z * LOG2E)); }
;     static __device__ __forceinline__ unsigned q8(float z) { return (unsigned)(fast_sigmoid(z) * 255.f + 0.5f); }
;     __device__ __forceinline__ void operator()(const f32x4 (&acc)[2][2][4][2], const g8::Unit& u, int wr, int wc, int fr, int fq) const {
;         const int row0 = u.pm * 256 + wr * 64 + fr, col0 = u.pn * 256 + wc * 32 + 8 * fq;
; #pragma unroll
;         for (int bj = 0; bj < 2; ++bj) {
;             const f32x4 bv0 = *(const f32x4*)(bgate + col0 + bj * 128), bv1 = *(const f32x4*)(bgate + col0 + bj * 128 + 4);
; #pragma unroll
;             for (int ai = 0; ai < 2; ++ai)
; #pragma unroll
;                 for (int m = 0; m < 4; ++m) { const int row = row0 + ai * 128 + m * 16; unsigned char* rp = GT + (size_t)row * 4096 + col0 + bj * 128;
;                     const f32x4 v0 = acc[ai][bj][m][0] * 0.03125f + bv0, v1 = acc[ai][bj][m][1] * 0.03125f + bv1;
;                     u32x2 w; w.x = q8(v0[0]) | (q8(v0[1]) << 8) | (q8(v0[2]) << 16) | (q8(v0[3]) << 24); w.y = q8(v1[0]) | (q8(v1[1]) << 8) | (q8(v1[2]) << 16) | (q8(v1[3]) << 24);
;                     *(u32x2*)rp = w; } }
	global_store_dwordx2 v[196:197], v[96:97], off
	global_store_dwordx2 v[198:199], v[88:89], off
	v_pk_fma_f32 v[64:65], v[64:65], s[20:21], v[184:185] op_sel_hi:[1,0,1]
	v_pk_fma_f32 v[66:67], v[66:67], s[20:21], v[186:187] op_sel_hi:[1,0,1]
	v_pk_fma_f32 v[60:61], v[60:61], s[20:21], v[188:189] op_sel_hi:[1,0,1]
	v_pk_fma_f32 v[62:63], v[62:63], s[20:21], v[190:191] op_sel_hi:[1,0,1]
	v_pk_fma_f32 v[56:57], v[56:57], s[20:21], v[184:185] op_sel_hi:[1,0,1]
	v_pk_fma_f32 v[58:59], v[58:59], s[20:21], v[186:187] op_sel_hi:[1,0,1]
	v_pk_fma_f32 v[52:53], v[52:53], s[20:21], v[188:189] op_sel_hi:[1,0,1]
	v_pk_fma_f32 v[54:55], v[54:55], s[20:21], v[190:191] op_sel_hi:[1,0,1]
	v_exp_f32_e32 v64, v64
	v_exp_f32_e32 v65, v65
	v_exp_f32_e32 v66, v66
	v_exp_f32_e32 v67, v67
	v_exp_f32_e32 v60, v60
	v_exp_f32_e32 v61, v61
	v_exp_f32_e32 v62, v62
	v_exp_f32_e32 v63, v63
	v_exp_f32_e32 v56, v56
	v_exp_f32_e32 v57, v57
	v_exp_f32_e32 v58, v58
	v_exp_f32_e32 v59, v59
	v_exp_f32_e32 v52, v52
	v_exp_f32_e32 v53, v53
	v_exp_f32_e32 v54, v54
	v_exp_f32_e32 v55, v55
	v_fma_f32 v64, v64, s21, s21
	v_fma_f32 v65, v65, s21, s21
	v_fma_f32 v66, v66, s21, s21
	v_fma_f32 v67, v67, s21, s21
	v_fma_f32 v60, v60, s21, s21
	v_fma_f32 v61, v61, s21, s21
	v_fma_f32 v62, v62, s21, s21
	v_fma_f32 v63, v63, s21, s21
	v_fma_f32 v56, v56, s21, s21
	v_fma_f32 v57, v57, s21, s21
	v_fma_f32 v58, v58, s21, s21
	v_fma_f32 v59, v59, s21, s21
	v_fma_f32 v52, v52, s21, s21
	v_fma_f32 v53, v53, s21, s21
	v_fma_f32 v54, v54, s21, s21
	v_fma_f32 v55, v55, s21, s21
	v_rcp_f32_e32 v64, v64
	v_rcp_f32_e32 v65, v65
	v_rcp_f32_e32 v66, v66
	v_rcp_f32_e32 v67, v67
	v_rcp_f32_e32 v60, v60
	v_rcp_f32_e32 v61, v61
	v_rcp_f32_e32 v62, v62
	v_rcp_f32_e32 v63, v63
	v_rcp_f32_e32 v56, v56
	v_rcp_f32_e32 v57, v57
	v_rcp_f32_e32 v58, v58
	v_rcp_f32_e32 v59, v59
	v_rcp_f32_e32 v52, v52
	v_rcp_f32_e32 v53, v53
	v_rcp_f32_e32 v54, v54
	v_rcp_f32_e32 v55, v55
	v_cvt_rpi_i32_f32_e32 v64, v64
	v_cvt_rpi_i32_f32_e32 v56, v56
	v_cvt_rpi_i32_f32_sdwa v64, v65 dst_sel:BYTE_1 dst_unused:UNUSED_PRESERVE src0_sel:DWORD
	v_cvt_rpi_i32_f32_sdwa v56, v57 dst_sel:BYTE_1 dst_unused:UNUSED_PRESERVE src0_sel:DWORD
	v_cvt_rpi_i32_f32_e32 v65, v60
	v_cvt_rpi_i32_f32_e32 v57, v52
	v_cvt_rpi_i32_f32_sdwa v64, v66 dst_sel:BYTE_2 dst_unused:UNUSED_PRESERVE src0_sel:DWORD
	v_cvt_rpi_i32_f32_sdwa v56, v58 dst_sel:BYTE_2 dst_unused:UNUSED_PRESERVE src0_sel:DWORD
	v_cvt_rpi_i32_f32_sdwa v65, v61 dst_sel:BYTE_1 dst_unused:UNUSED_PRESERVE src0_sel:DWORD
	v_cvt_rpi_i32_f32_sdwa v57, v53 dst_sel:BYTE_1 dst_unused:UNUSED_PRESERVE src0_sel:DWORD
	v_cvt_rpi_i32_f32_sdwa v64, v67 dst_sel:BYTE_3 dst_unused:UNUSED_PRESERVE src0_sel:DWORD
	v_cvt_rpi_i32_f32_sdwa v56, v59 dst_sel:BYTE_3 dst_unused:UNUSED_PRESERVE src0_sel:DWORD
	v_cvt_rpi_i32_f32_sdwa v65, v62 dst_sel:BYTE_2 dst_unused:UNUSED_PRESERVE src0_sel:DWORD
	v_cvt_rpi_i32_f32_sdwa v57, v54 dst_sel:BYTE_2 dst_unused:UNUSED_PRESERVE src0_sel:DWORD
	v_cvt_rpi_i32_f32_sdwa v65, v63 dst_sel:BYTE_3 dst_unused:UNUSED_PRESERVE src0_sel:DWORD
	v_cvt_rpi_i32_f32_sdwa v57, v55 dst_sel:BYTE_3 dst_unused:UNUSED_PRESERVE src0_sel:DWORD
	ds_bpermute_b32 v64, v17, v64
	ds_bpermute_b32 v65, v17, v65
	ds_bpermute_b32 v56, v17, v56
	ds_bpermute_b32 v57, v17, v57
	s_waitcnt lgkmcnt(4)
	global_store_dwordx2 v[8:9], v[80:81], off offset:128
	global_store_dwordx2 v[10:11], v[72:73], off offset:128
	v_pk_fma_f32 v[48:49], v[48:49], s[20:21], v[184:185] op_sel_hi:[1,0,1]
	v_pk_fma_f32 v[50:51], v[50:51], s[20:21], v[186:187] op_sel_hi:[1,0,1]
	v_pk_fma_f32 v[44:45], v[44:45], s[20:21], v[188:189] op_sel_hi:[1,0,1]
	v_pk_fma_f32 v[46:47], v[46:47], s[20:21], v[190:191] op_sel_hi:[1,0,1]
	v_pk_fma_f32 v[40:41], v[40:41], s[20:21], v[184:185] op_sel_hi:[1,0,1]
	v_pk_fma_f32 v[42:43], v[42:43], s[20:21], v[186:187] op_sel_hi:[1,0,1]
	v_pk_fma_f32 v[36:37], v[36:37], s[20:21], v[188:189] op_sel_hi:[1,0,1]
	v_pk_fma_f32 v[38:39], v[38:39], s[20:21], v[190:191] op_sel_hi:[1,0,1]
	v_exp_f32_e32 v48, v48
	v_exp_f32_e32 v49, v49
	v_exp_f32_e32 v50, v50
	v_exp_f32_e32 v51, v51
	v_exp_f32_e32 v44, v44
	v_exp_f32_e32 v45, v45
	v_exp_f32_e32 v46, v46
	v_exp_f32_e32 v47, v47
	v_exp_f32_e32 v40, v40
	v_exp_f32_e32 v41, v41
	v_exp_f32_e32 v42, v42
	v_exp_f32_e32 v43, v43
	v_exp_f32_e32 v36, v36
	v_exp_f32_e32 v37, v37
	v_exp_f32_e32 v38, v38
	v_exp_f32_e32 v39, v39
	v_fma_f32 v48, v48, s21, s21
	v_fma_f32 v49, v49, s21, s21
	v_fma_f32 v50, v50, s21, s21
	v_fma_f32 v51, v51, s21, s21
	v_fma_f32 v44, v44, s21, s21
	v_fma_f32 v45, v45, s21, s21
	v_fma_f32 v46, v46, s21, s21
	v_fma_f32 v47, v47, s21, s21
	v_fma_f32 v40, v40, s21, s21
	v_fma_f32 v41, v41, s21, s21
	v_fma_f32 v42, v42, s21, s21
	v_fma_f32 v43, v43, s21, s21
	v_fma_f32 v36, v36, s21, s21
	v_fma_f32 v37, v37, s21, s21
	v_fma_f32 v38, v38, s21, s21
	v_fma_f32 v39, v39, s21, s21
	v_rcp_f32_e32 v48, v48
	v_rcp_f32_e32 v49, v49
	v_rcp_f32_e32 v50, v50
	v_rcp_f32_e32 v51, v51
	v_rcp_f32_e32 v44, v44
	v_rcp_f32_e32 v45, v45
	v_rcp_f32_e32 v46, v46
	v_rcp_f32_e32 v47, v47
	v_rcp_f32_e32 v40, v40
	v_rcp_f32_e32 v41, v41
	v_rcp_f32_e32 v42, v42
	v_rcp_f32_e32 v43, v43
	v_rcp_f32_e32 v36, v36
	v_rcp_f32_e32 v37, v37
	v_rcp_f32_e32 v38, v38
	v_rcp_f32_e32 v39, v39
	v_cvt_rpi_i32_f32_e32 v48, v48
	v_cvt_rpi_i32_f32_e32 v40, v40
	v_cvt_rpi_i32_f32_sdwa v48, v49 dst_sel:BYTE_1 dst_unused:UNUSED_PRESERVE src0_sel:DWORD
	v_cvt_rpi_i32_f32_sdwa v40, v41 dst_sel:BYTE_1 dst_unused:UNUSED_PRESERVE src0_sel:DWORD
	v_cvt_rpi_i32_f32_e32 v49, v44
	v_cvt_rpi_i32_f32_e32 v41, v36
	v_cvt_rpi_i32_f32_sdwa v48, v50 dst_sel:BYTE_2 dst_unused:UNUSED_PRESERVE src0_sel:DWORD
	v_cvt_rpi_i32_f32_sdwa v40, v42 dst_sel:BYTE_2 dst_unused:UNUSED_PRESERVE src0_sel:DWORD
	v_cvt_rpi_i32_f32_sdwa v49, v45 dst_sel:BYTE_1 dst_unused:UNUSED_PRESERVE src0_sel:DWORD
	v_cvt_rpi_i32_f32_sdwa v41, v37 dst_sel:BYTE_1 dst_unused:UNUSED_PRESERVE src0_sel:DWORD
	v_cvt_rpi_i32_f32_sdwa v48, v51 dst_sel:BYTE_3 dst_unused:UNUSED_PRESERVE src0_sel:DWORD
	v_cvt_rpi_i32_f32_sdwa v40, v43 dst_sel:BYTE_3 dst_unused:UNUSED_PRESERVE src0_sel:DWORD
	v_cvt_rpi_i32_f32_sdwa v49, v46 dst_sel:BYTE_2 dst_unused:UNUSED_PRESERVE src0_sel:DWORD
	v_cvt_rpi_i32_f32_sdwa v41, v38 dst_sel:BYTE_2 dst_unused:UNUSED_PRESERVE src0_sel:DWORD
	v_cvt_rpi_i32_f32_sdwa v49, v47 dst_sel:BYTE_3 dst_unused:UNUSED_PRESERVE src0_sel:DWORD
	v_cvt_rpi_i32_f32_sdwa v41, v39 dst_sel:BYTE_3 dst_unused:UNUSED_PRESERVE src0_sel:DWORD
	ds_bpermute_b32 v48, v17, v48
	ds_bpermute_b32 v49, v17, v49
	ds_bpermute_b32 v40, v17, v40
	ds_bpermute_b32 v41, v17, v41
	s_waitcnt lgkmcnt(4)
; __device__ __forceinline__ float fast_sigmoid(float z) { return __builtin_amdgcn_rcpf(1.f + __builtin_amdgcn_exp2f(-z * LOG2E)); }
;     static __device__ __forceinline__ unsigned q8(float z) { return (unsigned)(fast_sigmoid(z) * 255.f + 0.5f); }
;     __device__ __forceinline__ void operator()(const f32x4 (&acc)[2][2][4][2], const g8::Unit& u, int wr, int wc, int fr, int fq) const {
;         const int row0 = u.pm * 256 + wr * 64 + fr, col0 = u.pn * 256 + wc * 32 + 8 * fq;
; #pragma unroll
;         for (int bj = 0; bj < 2; ++bj) {
;             const f32x4 bv0 = *(const f32x4*)(bgate + col0 + bj * 128), bv1 = *(const f32x4*)(bgate + col0 + bj * 128 + 4);
; #pragma unroll
;             for (int ai = 0; ai < 2; ++ai)
; #pragma unroll
;                 for (int m = 0; m < 4; ++m) { const int row = row0 + ai * 128 + m * 16; unsigned char* rp = GT + (size_t)row * 4096 + col0 + bj * 128;
;                     const f32x4 v0 = acc[ai][bj][m][0] * 0.03125f + bv0, v1 = acc[ai][bj][m][1] * 0.03125f + bv1;
;                     u32x2 w; w.x = q8(v0[0]) | (q8(v0[1]) << 8) | (q8(v0[2]) << 16) | (q8(v0[3]) << 24); w.y = q8(v1[0]) | (q8(v1[1]) << 8) | (q8(v1[2]) << 16) | (q8(v1[3]) << 24);
;                     *(u32x2*)rp = w; } }
	global_store_dwordx2 v[14:15], v[64:65], off offset:128
	global_store_dwordx2 v[168:169], v[56:57], off offset:128
	v_pk_fma_f32 v[32:33], v[32:33], s[20:21], v[184:185] op_sel_hi:[1,0,1]
	v_pk_fma_f32 v[34:35], v[34:35], s[20:21], v[186:187] op_sel_hi:[1,0,1]
	v_pk_fma_f32 v[26:27], v[26:27], s[20:21], v[188:189] op_sel_hi:[1,0,1]
	v_pk_fma_f32 v[28:29], v[28:29], s[20:21], v[190:191] op_sel_hi:[1,0,1]
	v_pk_fma_f32 v[22:23], v[22:23], s[20:21], v[184:185] op_sel_hi:[1,0,1]
	v_pk_fma_f32 v[24:25], v[24:25], s[20:21], v[186:187] op_sel_hi:[1,0,1]
	v_pk_fma_f32 v[18:19], v[18:19], s[20:21], v[188:189] op_sel_hi:[1,0,1]
	v_pk_fma_f32 v[20:21], v[20:21], s[20:21], v[190:191] op_sel_hi:[1,0,1]
	v_exp_f32_e32 v32, v32
	v_exp_f32_e32 v33, v33
	v_exp_f32_e32 v34, v34
	v_exp_f32_e32 v35, v35
	v_exp_f32_e32 v26, v26
	v_exp_f32_e32 v27, v27
	v_exp_f32_e32 v28, v28
	v_exp_f32_e32 v29, v29
	v_exp_f32_e32 v22, v22
	v_exp_f32_e32 v23, v23
	v_exp_f32_e32 v24, v24
	v_exp_f32_e32 v25, v25
	v_exp_f32_e32 v18, v18
	v_exp_f32_e32 v19, v19
	v_exp_f32_e32 v20, v20
	v_exp_f32_e32 v21, v21
	v_fma_f32 v32, v32, s21, s21
	v_fma_f32 v33, v33, s21, s21
	v_fma_f32 v34, v34, s21, s21
	v_fma_f32 v35, v35, s21, s21
	v_fma_f32 v26, v26, s21, s21
	v_fma_f32 v27, v27, s21, s21
	v_fma_f32 v28, v28, s21, s21
	v_fma_f32 v29, v29, s21, s21
	v_fma_f32 v22, v22, s21, s21
	v_fma_f32 v23, v23, s21, s21
	v_fma_f32 v24, v24, s21, s21
	v_fma_f32 v25, v25, s21, s21
	v_fma_f32 v18, v18, s21, s21
	v_fma_f32 v19, v19, s21, s21
	v_fma_f32 v20, v20, s21, s21
	v_fma_f32 v21, v21, s21, s21
	v_rcp_f32_e32 v32, v32
	v_rcp_f32_e32 v33, v33
	v_rcp_f32_e32 v34, v34
	v_rcp_f32_e32 v35, v35
	v_rcp_f32_e32 v26, v26
	v_rcp_f32_e32 v27, v27
	v_rcp_f32_e32 v28, v28
	v_rcp_f32_e32 v29, v29
	v_rcp_f32_e32 v22, v22
	v_rcp_f32_e32 v23, v23
	v_rcp_f32_e32 v24, v24
	v_rcp_f32_e32 v25, v25
	v_rcp_f32_e32 v18, v18
	v_rcp_f32_e32 v19, v19
	v_rcp_f32_e32 v20, v20
	v_rcp_f32_e32 v21, v21
	v_cvt_rpi_i32_f32_e32 v32, v32
	v_cvt_rpi_i32_f32_e32 v22, v22
	v_cvt_rpi_i32_f32_sdwa v32, v33 dst_sel:BYTE_1 dst_unused:UNUSED_PRESERVE src0_sel:DWORD
	v_cvt_rpi_i32_f32_sdwa v22, v23 dst_sel:BYTE_1 dst_unused:UNUSED_PRESERVE src0_sel:DWORD
	v_cvt_rpi_i32_f32_e32 v33, v26
	v_cvt_rpi_i32_f32_e32 v23, v18
	v_cvt_rpi_i32_f32_sdwa v32, v34 dst_sel:BYTE_2 dst_unused:UNUSED_PRESERVE src0_sel:DWORD
	v_cvt_rpi_i32_f32_sdwa v22, v24 dst_sel:BYTE_2 dst_unused:UNUSED_PRESERVE src0_sel:DWORD
	v_cvt_rpi_i32_f32_sdwa v33, v27 dst_sel:BYTE_1 dst_unused:UNUSED_PRESERVE src0_sel:DWORD
	v_cvt_rpi_i32_f32_sdwa v23, v19 dst_sel:BYTE_1 dst_unused:UNUSED_PRESERVE src0_sel:DWORD
	v_cvt_rpi_i32_f32_sdwa v32, v35 dst_sel:BYTE_3 dst_unused:UNUSED_PRESERVE src0_sel:DWORD
	v_cvt_rpi_i32_f32_sdwa v22, v25 dst_sel:BYTE_3 dst_unused:UNUSED_PRESERVE src0_sel:DWORD
	v_cvt_rpi_i32_f32_sdwa v33, v28 dst_sel:BYTE_2 dst_unused:UNUSED_PRESERVE src0_sel:DWORD
	v_cvt_rpi_i32_f32_sdwa v23, v20 dst_sel:BYTE_2 dst_unused:UNUSED_PRESERVE src0_sel:DWORD
	v_cvt_rpi_i32_f32_sdwa v33, v29 dst_sel:BYTE_3 dst_unused:UNUSED_PRESERVE src0_sel:DWORD
	v_cvt_rpi_i32_f32_sdwa v23, v21 dst_sel:BYTE_3 dst_unused:UNUSED_PRESERVE src0_sel:DWORD
	ds_bpermute_b32 v32, v17, v32
	ds_bpermute_b32 v33, v17, v33
	ds_bpermute_b32 v22, v17, v22
	ds_bpermute_b32 v23, v17, v23
	s_waitcnt lgkmcnt(4)
	global_store_dwordx2 v[192:193], v[48:49], off offset:128
	global_store_dwordx2 v[194:195], v[40:41], off offset:128
	s_waitcnt lgkmcnt(0)
	global_store_dwordx2 v[196:197], v[32:33], off offset:128
	global_store_dwordx2 v[198:199], v[22:23], off offset:128
	s_mov_b64 s[52:53], -1
	s_andn2_b64 vcc, exec, s[16:17]
	s_cbranch_vccnz .LBB0_1080
	s_and_b64 vcc, exec, s[40:41]
	s_cbranch_vccnz .LBB0_1079
	s_barrier
	s_branch .LBB0_1079
